# baseline (speedup 1.0000x reference)
.LBB3_35:
	s_andn2_b64 vcc, exec, s[2:3]
	s_cbranch_vccnz .LBB3_39
	s_waitcnt vmcnt(4)
	v_ashrrev_i32_e32 v81, 31, v80
	v_lshl_add_u64 v[2:3], v[80:81], 3, s[20:21]
	v_add_co_u32_e32 v2, vcc, 0x48000, v2
	s_movk_i32 s8, 0x620
	s_nop 0
	v_addc_co_u32_e32 v3, vcc, 0, v3, vcc
	global_load_dwordx2 v[82:83], v[2:3], off
	v_and_b32_e32 v2, 0x70, v7
	v_bitop3_b32 v2, v0, v2, 48 bitop3:0x6c
	s_waitcnt vmcnt(4)
	v_mad_u64_u32 v[64:65], s[6:7], v9, s8, v[2:3]
	v_lshrrev_b32_e32 v3, 4, v92
	v_bitop3_b32 v3, v3, v0, 4 bitop3:0x36
	v_lshlrev_b32_e32 v3, 4, v3
	v_and_b32_e32 v4, 0x70, v3
	s_waitcnt vmcnt(3)
	v_mad_u64_u32 v[66:67], s[6:7], v8, s8, v[4:5]
	s_waitcnt vmcnt(2)
	v_mad_u64_u32 v[68:69], s[6:7], v6, s8, v[2:3]
	s_waitcnt vmcnt(1)
	v_mad_u64_u32 v[70:71], s[6:7], v1, s8, v[4:5]
	v_lshrrev_b32_e32 v85, 5, v92
	v_bfe_u32 v2, v0, 1, 3
	s_mov_b64 s[6:7], 0x1800
	s_add_u32 s4, s20, 0x4000000
	v_bitop3_b32 v32, v85, v2, 2 bitop3:0x36
	v_bitop3_b32 v33, v85, v2, 4 bitop3:0x36
	v_bitop3_b32 v34, v85, v2, 6 bitop3:0x36
	v_lshl_add_u64 v[2:3], v[86:87], 0, s[6:7]
	s_addc_u32 s5, s21, 0
	s_lshl_b32 s2, s27, 12
	s_addk_i32 s2, 0x6000
	v_lshrrev_b32_e32 v1, 1, v0
	v_or_b32_e32 v81, s2, v84
	v_lshlrev_b32_e32 v0, 7, v0
	v_and_b32_e32 v8, 0xf80, v0
	v_lshlrev_b32_e32 v9, 4, v32
	v_bitop3_b32 v1, v85, v1, 7 bitop3:0x78
	v_or3_b32 v96, s2, v9, v8
	v_lshlrev_b32_e32 v9, 4, v33
	v_lshlrev_b32_e32 v1, 4, v1
	v_or3_b32 v97, s2, v9, v8
	v_lshlrev_b32_e32 v9, 4, v34
	v_or3_b32 v95, s2, v1, v8
	v_or3_b32 v94, s2, v9, v8
	v_add_u32_e32 v98, 0x103c0, v84
	global_load_dwordx4 v[116:119], v64, s[4:5] offset:0
	global_load_dwordx4 v[120:123], v66, s[4:5] offset:0
	global_load_dwordx4 v[124:127], v68, s[4:5] offset:0
	global_load_dwordx4 v[128:131], v70, s[4:5] offset:0
	global_load_dwordx4 v[132:135], v64, s[4:5] offset:128
	global_load_dwordx4 v[136:139], v66, s[4:5] offset:128
	global_load_dwordx4 v[140:143], v68, s[4:5] offset:128
	global_load_dwordx4 v[144:147], v70, s[4:5] offset:128
	global_load_dwordx4 v[148:151], v64, s[4:5] offset:256
	global_load_dwordx4 v[152:155], v66, s[4:5] offset:256
	global_load_dwordx4 v[156:159], v68, s[4:5] offset:256
	global_load_dwordx4 v[72:75], v70, s[4:5] offset:256
	s_add_u32 m0, s46, 0x0
	s_nop 0
	global_load_lds_dwordx4 v76, s[40:41]
	s_add_u32 m0, s47, 0x0
	s_nop 0
	global_load_lds_dwordx4 v77, s[42:43]
	s_add_u32 m0, s48, 0x0
	s_nop 0
	global_load_lds_dwordx4 v78, s[44:45]
	s_add_u32 m0, s46, 0x3000
	s_add_u32 s40, s40, 0x1800
	s_addc_u32 s41, s41, 0
	global_load_lds_dwordx4 v76, s[40:41]
	s_add_u32 m0, s47, 0x3000
	s_add_u32 s42, s42, 0x1800
	s_addc_u32 s43, s43, 0
	global_load_lds_dwordx4 v77, s[42:43]
	s_add_u32 m0, s48, 0x3000
	s_add_u32 s44, s44, 0x1800
	s_addc_u32 s45, s45, 0
	global_load_lds_dwordx4 v78, s[44:45]
	s_add_u32 m0, s46, 0xd3c0
	s_add_u32 s40, s40, 0x1800
	s_addc_u32 s41, s41, 0
	global_load_lds_dwordx4 v76, s[40:41]
	s_add_u32 m0, s47, 0xd3c0
	s_add_u32 s42, s42, 0x1800
	s_addc_u32 s43, s43, 0
	global_load_lds_dwordx4 v77, s[42:43]
	s_add_u32 m0, s48, 0xd3c0
	s_add_u32 s44, s44, 0x1800
	s_addc_u32 s45, s45, 0
	global_load_lds_dwordx4 v78, s[44:45]
	s_add_u32 m0, s46, 0x103c0
	s_add_u32 s40, s40, 0x1800
	s_addc_u32 s41, s41, 0
	global_load_lds_dwordx4 v76, s[40:41]
	s_add_u32 m0, s47, 0x103c0
	s_add_u32 s42, s42, 0x1800
	s_addc_u32 s43, s43, 0
	global_load_lds_dwordx4 v77, s[42:43]
	s_add_u32 m0, s48, 0x103c0
	s_add_u32 s44, s44, 0x1800
	s_addc_u32 s45, s45, 0
	global_load_lds_dwordx4 v78, s[44:45]
	s_waitcnt vmcnt(20)
	ds_write_b128 v81, v[116:119]
	ds_write_b128 v81, v[120:123] offset:1024
	ds_write_b128 v81, v[124:127] offset:2048
	ds_write_b128 v81, v[128:131] offset:3072
	ds_read_b128 v[52:55], v95
	ds_read_b128 v[56:59], v96
	ds_read_b128 v[60:63], v97
	ds_read_b128 v[0:3], v94
	global_load_dwordx4 v[116:119], v64, s[4:5] offset:384
	global_load_dwordx4 v[120:123], v66, s[4:5] offset:384
	global_load_dwordx4 v[124:127], v68, s[4:5] offset:384
	global_load_dwordx4 v[128:131], v70, s[4:5] offset:384
	s_waitcnt vmcnt(13)
	s_waitcnt lgkmcnt(0)
	s_barrier
	ds_read_b128 v[4:7], v84 offset:0
	ds_read_b128 v[8:11], v84 offset:1024
	ds_read_b128 v[12:15], v84 offset:2048
	ds_read_b128 v[16:19], v84 offset:3072
	ds_read_b128 v[20:23], v84 offset:4096
	ds_read_b128 v[24:27], v84 offset:5120
	ds_read_b128 v[28:31], v84 offset:6144
	ds_read_b128 v[32:35], v84 offset:7168
	ds_read_b128 v[36:39], v84 offset:8192
	ds_read_b128 v[40:43], v84 offset:9216
	ds_read_b128 v[44:47], v84 offset:10240
	ds_read_b128 v[48:51], v84 offset:11264
	s_waitcnt lgkmcnt(6)
	v_mfma_f32_32x32x16_f16 a[80:95], v[4:7], v[52:55], 0
	s_waitcnt vmcnt(20)
	ds_write_b128 v81, v[132:135]
	ds_write_b128 v81, v[136:139] offset:1024
	v_mfma_f32_32x32x16_f16 a[64:79], v[8:11], v[52:55], 0
	ds_write_b128 v81, v[140:143] offset:2048
	ds_write_b128 v81, v[144:147] offset:3072
	v_mfma_f32_32x32x16_f16 a[48:63], v[12:15], v[52:55], 0
	ds_read_b128 v[100:103], v95
	ds_read_b128 v[104:107], v96
	ds_read_b128 v[108:111], v97
	ds_read_b128 v[112:115], v94
	s_waitcnt vmcnt(10)
	s_waitcnt lgkmcnt(8)
	s_barrier
	ds_read_b128 v[4:7], v84 offset:12288
	ds_read_b128 v[8:11], v84 offset:13312
	ds_read_b128 v[12:15], v84 offset:14336
	v_mfma_f32_32x32x16_f16 a[32:47], v[16:19], v[52:55], 0
	ds_read_b128 v[16:19], v84 offset:15360
	v_mfma_f32_32x32x16_f16 a[16:31], v[20:23], v[52:55], 0
	ds_read_b128 v[20:23], v84 offset:16384
	v_mfma_f32_32x32x16_f16 a[0:15], v[24:27], v[52:55], 0
	ds_read_b128 v[24:27], v84 offset:17408
	s_waitcnt lgkmcnt(6)
	v_mfma_f32_32x32x16_f16 a[80:95], v[28:31], v[56:59], a[80:95]
	s_add_u32 m0, s46, 0x0
	s_add_u32 s40, s40, 0x1800
	s_addc_u32 s41, s41, 0
	global_load_lds_dwordx4 v76, s[40:41]
	ds_read_b128 v[28:31], v84 offset:18432
	v_mfma_f32_32x32x16_f16 a[64:79], v[32:35], v[56:59], a[64:79]
	global_load_dwordx4 v[132:135], v64, s[4:5] offset:512
	global_load_dwordx4 v[136:139], v66, s[4:5] offset:512
	ds_read_b128 v[32:35], v84 offset:19456
	v_mfma_f32_32x32x16_f16 a[48:63], v[36:39], v[56:59], a[48:63]
	s_add_u32 m0, s47, 0x0
	s_add_u32 s42, s42, 0x1800
	s_addc_u32 s43, s43, 0
	global_load_lds_dwordx4 v77, s[42:43]
	ds_read_b128 v[36:39], v84 offset:20480
	v_mfma_f32_32x32x16_f16 a[32:47], v[40:43], v[56:59], a[32:47]
	global_load_dwordx4 v[140:143], v68, s[4:5] offset:512
	global_load_dwordx4 v[144:147], v70, s[4:5] offset:512
	ds_read_b128 v[40:43], v84 offset:21504
	v_mfma_f32_32x32x16_f16 a[16:31], v[44:47], v[56:59], a[16:31]
	s_add_u32 m0, s48, 0x0
	s_add_u32 s44, s44, 0x1800
	s_addc_u32 s45, s45, 0
	global_load_lds_dwordx4 v78, s[44:45]
	ds_read_b128 v[44:47], v84 offset:22528
	v_mfma_f32_32x32x16_f16 a[0:15], v[48:51], v[56:59], a[0:15]
	ds_read_b128 v[48:51], v84 offset:23552
	s_waitcnt lgkmcnt(6)
	v_mfma_f32_32x32x16_f16 a[80:95], v[4:7], v[60:63], a[80:95]
	v_mfma_f32_32x32x16_f16 a[64:79], v[8:11], v[60:63], a[64:79]
	v_mfma_f32_32x32x16_f16 a[48:63], v[12:15], v[60:63], a[48:63]
	s_waitcnt vmcnt(14)
	s_waitcnt lgkmcnt(0)
	s_barrier
	ds_read_b128 v[4:7], v84 offset:54208
	ds_read_b128 v[8:11], v84 offset:55232
	ds_read_b128 v[12:15], v84 offset:56256
	v_mfma_f32_32x32x16_f16 a[32:47], v[16:19], v[60:63], a[32:47]
	ds_read_b128 v[16:19], v84 offset:57280
	v_mfma_f32_32x32x16_f16 a[16:31], v[20:23], v[60:63], a[16:31]
	ds_read_b128 v[20:23], v84 offset:58304
	v_mfma_f32_32x32x16_f16 a[0:15], v[24:27], v[60:63], a[0:15]
	ds_read_b128 v[24:27], v84 offset:59328
	v_mfma_f32_32x32x16_f16 a[80:95], v[28:31], v[0:3], a[80:95]
	s_add_u32 m0, s46, 0x3000
	s_add_u32 s40, s40, 0x1800
	s_addc_u32 s41, s41, 0
	global_load_lds_dwordx4 v76, s[40:41]
	ds_read_b128 v[28:31], v84 offset:60352
	v_mfma_f32_32x32x16_f16 a[64:79], v[32:35], v[0:3], a[64:79]
	ds_read_b128 v[32:35], v84 offset:61376
	v_mfma_f32_32x32x16_f16 a[48:63], v[36:39], v[0:3], a[48:63]
	s_add_u32 m0, s47, 0x3000
	s_add_u32 s42, s42, 0x1800
	s_addc_u32 s43, s43, 0
	global_load_lds_dwordx4 v77, s[42:43]
	ds_read_b128 v[36:39], v84 offset:62400
	v_mfma_f32_32x32x16_f16 a[32:47], v[40:43], v[0:3], a[32:47]
	ds_read_b128 v[40:43], v84 offset:63424
	v_mfma_f32_32x32x16_f16 a[16:31], v[44:47], v[0:3], a[16:31]
	s_add_u32 m0, s48, 0x3000
	s_add_u32 s44, s44, 0x1800
	s_addc_u32 s45, s45, 0
	global_load_lds_dwordx4 v78, s[44:45]
	ds_read_b128 v[44:47], v84 offset:64448
	v_mfma_f32_32x32x16_f16 a[0:15], v[48:51], v[0:3], a[0:15]
	ds_read_b128 v[48:51], v84 offset:65472
	s_waitcnt lgkmcnt(6)
	v_mfma_f32_32x32x16_f16 a[80:95], v[4:7], v[100:103], a[80:95]
	s_waitcnt vmcnt(26)
	ds_write_b128 v81, v[148:151]
	ds_write_b128 v81, v[152:155] offset:1024
	v_mfma_f32_32x32x16_f16 a[64:79], v[8:11], v[100:103], a[64:79]
	ds_write_b128 v81, v[156:159] offset:2048
	ds_write_b128 v81, v[72:75] offset:3072
	v_mfma_f32_32x32x16_f16 a[48:63], v[12:15], v[100:103], a[48:63]
	ds_read_b128 v[52:55], v95
	ds_read_b128 v[56:59], v96
	ds_read_b128 v[60:63], v97
	ds_read_b128 v[0:3], v94
	s_waitcnt vmcnt(14)
	s_waitcnt lgkmcnt(8)
	s_barrier
	ds_read_b128 v[4:7], v98
	ds_read_b128 v[8:11], v98 offset:1024
	ds_read_b128 v[12:15], v98 offset:2048
	v_mfma_f32_32x32x16_f16 a[32:47], v[16:19], v[100:103], a[32:47]
	ds_read_b128 v[16:19], v98 offset:3072
	v_mfma_f32_32x32x16_f16 a[16:31], v[20:23], v[100:103], a[16:31]
	ds_read_b128 v[20:23], v98 offset:4096
	v_mfma_f32_32x32x16_f16 a[0:15], v[24:27], v[100:103], a[0:15]
	ds_read_b128 v[24:27], v98 offset:5120
	s_waitcnt lgkmcnt(6)
	v_mfma_f32_32x32x16_f16 a[80:95], v[28:31], v[104:107], a[80:95]
	s_add_u32 m0, s46, 0xd3c0
	s_add_u32 s40, s40, 0x1800
	s_addc_u32 s41, s41, 0
	global_load_lds_dwordx4 v76, s[40:41]
	ds_read_b128 v[28:31], v98 offset:6144
	v_mfma_f32_32x32x16_f16 a[64:79], v[32:35], v[104:107], a[64:79]
	global_load_dwordx4 v[148:151], v64, s[4:5] offset:640
	global_load_dwordx4 v[152:155], v66, s[4:5] offset:640
	ds_read_b128 v[32:35], v98 offset:7168
	v_mfma_f32_32x32x16_f16 a[48:63], v[36:39], v[104:107], a[48:63]
	s_add_u32 m0, s47, 0xd3c0
	s_add_u32 s42, s42, 0x1800
	s_addc_u32 s43, s43, 0
	global_load_lds_dwordx4 v77, s[42:43]
	ds_read_b128 v[36:39], v98 offset:8192
	v_mfma_f32_32x32x16_f16 a[32:47], v[40:43], v[104:107], a[32:47]
	global_load_dwordx4 v[156:159], v68, s[4:5] offset:640
	global_load_dwordx4 v[72:75], v70, s[4:5] offset:640
	ds_read_b128 v[40:43], v98 offset:9216
	v_mfma_f32_32x32x16_f16 a[16:31], v[44:47], v[104:107], a[16:31]
	s_add_u32 m0, s48, 0xd3c0
	s_add_u32 s44, s44, 0x1800
	s_addc_u32 s45, s45, 0
	global_load_lds_dwordx4 v78, s[44:45]
	ds_read_b128 v[44:47], v98 offset:10240
	v_mfma_f32_32x32x16_f16 a[0:15], v[48:51], v[104:107], a[0:15]
	ds_read_b128 v[48:51], v98 offset:11264
	s_waitcnt lgkmcnt(6)
	v_mfma_f32_32x32x16_f16 a[80:95], v[4:7], v[108:111], a[80:95]
	v_mfma_f32_32x32x16_f16 a[64:79], v[8:11], v[108:111], a[64:79]
	v_mfma_f32_32x32x16_f16 a[48:63], v[12:15], v[108:111], a[48:63]
	s_waitcnt vmcnt(10)
	s_waitcnt lgkmcnt(0)
	s_barrier
	ds_read_b128 v[4:7], v84 offset:0
	ds_read_b128 v[8:11], v84 offset:1024
	ds_read_b128 v[12:15], v84 offset:2048
	v_mfma_f32_32x32x16_f16 a[32:47], v[16:19], v[108:111], a[32:47]
	ds_read_b128 v[16:19], v84 offset:3072
	v_mfma_f32_32x32x16_f16 a[16:31], v[20:23], v[108:111], a[16:31]
	ds_read_b128 v[20:23], v84 offset:4096
	v_mfma_f32_32x32x16_f16 a[0:15], v[24:27], v[108:111], a[0:15]
	ds_read_b128 v[24:27], v84 offset:5120
	v_mfma_f32_32x32x16_f16 a[80:95], v[28:31], v[112:115], a[80:95]
	s_add_u32 m0, s46, 0x103c0
	s_add_u32 s40, s40, 0x1800
	s_addc_u32 s41, s41, 0
	global_load_lds_dwordx4 v76, s[40:41]
	ds_read_b128 v[28:31], v84 offset:6144
	v_mfma_f32_32x32x16_f16 a[64:79], v[32:35], v[112:115], a[64:79]
	ds_read_b128 v[32:35], v84 offset:7168
	v_mfma_f32_32x32x16_f16 a[48:63], v[36:39], v[112:115], a[48:63]
	s_add_u32 m0, s47, 0x103c0
	s_add_u32 s42, s42, 0x1800
	s_addc_u32 s43, s43, 0
	global_load_lds_dwordx4 v77, s[42:43]
	ds_read_b128 v[36:39], v84 offset:8192
	v_mfma_f32_32x32x16_f16 a[32:47], v[40:43], v[112:115], a[32:47]
	ds_read_b128 v[40:43], v84 offset:9216
	v_mfma_f32_32x32x16_f16 a[16:31], v[44:47], v[112:115], a[16:31]
	s_add_u32 m0, s48, 0x103c0
	s_add_u32 s44, s44, 0x1800
	s_addc_u32 s45, s45, 0
	global_load_lds_dwordx4 v78, s[44:45]
	ds_read_b128 v[44:47], v84 offset:10240
	v_mfma_f32_32x32x16_f16 a[0:15], v[48:51], v[112:115], a[0:15]
	ds_read_b128 v[48:51], v84 offset:11264
	s_waitcnt lgkmcnt(6)
	v_mfma_f32_32x32x16_f16 a[80:95], v[4:7], v[52:55], a[80:95]
	s_waitcnt vmcnt(20)
	ds_write_b128 v81, v[116:119]
	ds_write_b128 v81, v[120:123] offset:1024
	v_mfma_f32_32x32x16_f16 a[64:79], v[8:11], v[52:55], a[64:79]
	ds_write_b128 v81, v[124:127] offset:2048
	ds_write_b128 v81, v[128:131] offset:3072
	v_mfma_f32_32x32x16_f16 a[48:63], v[12:15], v[52:55], a[48:63]
	ds_read_b128 v[100:103], v95
	ds_read_b128 v[104:107], v96
	ds_read_b128 v[108:111], v97
	ds_read_b128 v[112:115], v94
	s_waitcnt vmcnt(10)
	s_waitcnt lgkmcnt(8)
	s_barrier
	ds_read_b128 v[4:7], v84 offset:12288
	ds_read_b128 v[8:11], v84 offset:13312
	ds_read_b128 v[12:15], v84 offset:14336
	v_mfma_f32_32x32x16_f16 a[32:47], v[16:19], v[52:55], a[32:47]
	ds_read_b128 v[16:19], v84 offset:15360
	v_mfma_f32_32x32x16_f16 a[16:31], v[20:23], v[52:55], a[16:31]
	ds_read_b128 v[20:23], v84 offset:16384
	v_mfma_f32_32x32x16_f16 a[0:15], v[24:27], v[52:55], a[0:15]
	ds_read_b128 v[24:27], v84 offset:17408
	s_waitcnt lgkmcnt(6)
	v_mfma_f32_32x32x16_f16 a[80:95], v[28:31], v[56:59], a[80:95]
	s_add_u32 m0, s46, 0x0
	s_add_u32 s40, s40, 0x1800
	s_addc_u32 s41, s41, 0
	global_load_lds_dwordx4 v76, s[40:41]
	ds_read_b128 v[28:31], v84 offset:18432
	v_mfma_f32_32x32x16_f16 a[64:79], v[32:35], v[56:59], a[64:79]
	global_load_dwordx4 v[116:119], v64, s[4:5] offset:768
	global_load_dwordx4 v[120:123], v66, s[4:5] offset:768
	ds_read_b128 v[32:35], v84 offset:19456
	v_mfma_f32_32x32x16_f16 a[48:63], v[36:39], v[56:59], a[48:63]
	s_add_u32 m0, s47, 0x0
	s_add_u32 s42, s42, 0x1800
	s_addc_u32 s43, s43, 0
	global_load_lds_dwordx4 v77, s[42:43]
	ds_read_b128 v[36:39], v84 offset:20480
	v_mfma_f32_32x32x16_f16 a[32:47], v[40:43], v[56:59], a[32:47]
	global_load_dwordx4 v[124:127], v68, s[4:5] offset:768
	global_load_dwordx4 v[128:131], v70, s[4:5] offset:768
	ds_read_b128 v[40:43], v84 offset:21504
	v_mfma_f32_32x32x16_f16 a[16:31], v[44:47], v[56:59], a[16:31]
	s_add_u32 m0, s48, 0x0
	s_add_u32 s44, s44, 0x1800
	s_addc_u32 s45, s45, 0
	global_load_lds_dwordx4 v78, s[44:45]
	ds_read_b128 v[44:47], v84 offset:22528
	v_mfma_f32_32x32x16_f16 a[0:15], v[48:51], v[56:59], a[0:15]
	ds_read_b128 v[48:51], v84 offset:23552
	s_waitcnt lgkmcnt(6)
	v_mfma_f32_32x32x16_f16 a[80:95], v[4:7], v[60:63], a[80:95]
	v_mfma_f32_32x32x16_f16 a[64:79], v[8:11], v[60:63], a[64:79]
	v_mfma_f32_32x32x16_f16 a[48:63], v[12:15], v[60:63], a[48:63]
	s_waitcnt vmcnt(10)
	s_waitcnt lgkmcnt(0)
	s_barrier
	ds_read_b128 v[4:7], v84 offset:54208
	ds_read_b128 v[8:11], v84 offset:55232
	ds_read_b128 v[12:15], v84 offset:56256
	v_mfma_f32_32x32x16_f16 a[32:47], v[16:19], v[60:63], a[32:47]
	ds_read_b128 v[16:19], v84 offset:57280
	v_mfma_f32_32x32x16_f16 a[16:31], v[20:23], v[60:63], a[16:31]
	ds_read_b128 v[20:23], v84 offset:58304
	v_mfma_f32_32x32x16_f16 a[0:15], v[24:27], v[60:63], a[0:15]
	ds_read_b128 v[24:27], v84 offset:59328
	v_mfma_f32_32x32x16_f16 a[80:95], v[28:31], v[0:3], a[80:95]
	s_add_u32 m0, s46, 0x3000
	s_add_u32 s40, s40, 0x1800
	s_addc_u32 s41, s41, 0
	global_load_lds_dwordx4 v76, s[40:41]
	ds_read_b128 v[28:31], v84 offset:60352
	v_mfma_f32_32x32x16_f16 a[64:79], v[32:35], v[0:3], a[64:79]
	ds_read_b128 v[32:35], v84 offset:61376
	v_mfma_f32_32x32x16_f16 a[48:63], v[36:39], v[0:3], a[48:63]
	s_add_u32 m0, s47, 0x3000
	s_add_u32 s42, s42, 0x1800
	s_addc_u32 s43, s43, 0
	global_load_lds_dwordx4 v77, s[42:43]
	ds_read_b128 v[36:39], v84 offset:62400
	v_mfma_f32_32x32x16_f16 a[32:47], v[40:43], v[0:3], a[32:47]
	ds_read_b128 v[40:43], v84 offset:63424
	v_mfma_f32_32x32x16_f16 a[16:31], v[44:47], v[0:3], a[16:31]
	s_add_u32 m0, s48, 0x3000
	s_add_u32 s44, s44, 0x1800
	s_addc_u32 s45, s45, 0
	global_load_lds_dwordx4 v78, s[44:45]
	ds_read_b128 v[44:47], v84 offset:64448
	v_mfma_f32_32x32x16_f16 a[0:15], v[48:51], v[0:3], a[0:15]
	ds_read_b128 v[48:51], v84 offset:65472
	s_waitcnt lgkmcnt(6)
	v_mfma_f32_32x32x16_f16 a[80:95], v[4:7], v[100:103], a[80:95]
	s_waitcnt vmcnt(24)
	ds_write_b128 v81, v[132:135]
	ds_write_b128 v81, v[136:139] offset:1024
	v_mfma_f32_32x32x16_f16 a[64:79], v[8:11], v[100:103], a[64:79]
	ds_write_b128 v81, v[140:143] offset:2048
	ds_write_b128 v81, v[144:147] offset:3072
	v_mfma_f32_32x32x16_f16 a[48:63], v[12:15], v[100:103], a[48:63]
	ds_read_b128 v[52:55], v95
	ds_read_b128 v[56:59], v96
	ds_read_b128 v[60:63], v97
	ds_read_b128 v[0:3], v94
	s_waitcnt vmcnt(10)
	s_waitcnt lgkmcnt(8)
	s_barrier
	ds_read_b128 v[4:7], v98
	ds_read_b128 v[8:11], v98 offset:1024
	ds_read_b128 v[12:15], v98 offset:2048
	v_mfma_f32_32x32x16_f16 a[32:47], v[16:19], v[100:103], a[32:47]
	ds_read_b128 v[16:19], v98 offset:3072
	v_mfma_f32_32x32x16_f16 a[16:31], v[20:23], v[100:103], a[16:31]
	ds_read_b128 v[20:23], v98 offset:4096
	v_mfma_f32_32x32x16_f16 a[0:15], v[24:27], v[100:103], a[0:15]
	ds_read_b128 v[24:27], v98 offset:5120
	s_waitcnt lgkmcnt(6)
	v_mfma_f32_32x32x16_f16 a[80:95], v[28:31], v[104:107], a[80:95]
	s_add_u32 m0, s46, 0xd3c0
	s_add_u32 s40, s40, 0x1800
	s_addc_u32 s41, s41, 0
	global_load_lds_dwordx4 v76, s[40:41]
	ds_read_b128 v[28:31], v98 offset:6144
	v_mfma_f32_32x32x16_f16 a[64:79], v[32:35], v[104:107], a[64:79]
	global_load_dwordx4 v[132:135], v64, s[4:5] offset:896
	global_load_dwordx4 v[136:139], v66, s[4:5] offset:896
	ds_read_b128 v[32:35], v98 offset:7168
	v_mfma_f32_32x32x16_f16 a[48:63], v[36:39], v[104:107], a[48:63]
	s_add_u32 m0, s47, 0xd3c0
	s_add_u32 s42, s42, 0x1800
	s_addc_u32 s43, s43, 0
	global_load_lds_dwordx4 v77, s[42:43]
	ds_read_b128 v[36:39], v98 offset:8192
	v_mfma_f32_32x32x16_f16 a[32:47], v[40:43], v[104:107], a[32:47]
	global_load_dwordx4 v[140:143], v68, s[4:5] offset:896
	global_load_dwordx4 v[144:147], v70, s[4:5] offset:896
	ds_read_b128 v[40:43], v98 offset:9216
	v_mfma_f32_32x32x16_f16 a[16:31], v[44:47], v[104:107], a[16:31]
	s_add_u32 m0, s48, 0xd3c0
	s_add_u32 s44, s44, 0x1800
	s_addc_u32 s45, s45, 0
	global_load_lds_dwordx4 v78, s[44:45]
	ds_read_b128 v[44:47], v98 offset:10240
	v_mfma_f32_32x32x16_f16 a[0:15], v[48:51], v[104:107], a[0:15]
	ds_read_b128 v[48:51], v98 offset:11264
	s_waitcnt lgkmcnt(6)
	v_mfma_f32_32x32x16_f16 a[80:95], v[4:7], v[108:111], a[80:95]
	v_mfma_f32_32x32x16_f16 a[64:79], v[8:11], v[108:111], a[64:79]
	v_mfma_f32_32x32x16_f16 a[48:63], v[12:15], v[108:111], a[48:63]
	s_waitcnt vmcnt(10)
	s_waitcnt lgkmcnt(0)
	s_barrier
	ds_read_b128 v[4:7], v84 offset:0
	ds_read_b128 v[8:11], v84 offset:1024
	ds_read_b128 v[12:15], v84 offset:2048
	v_mfma_f32_32x32x16_f16 a[32:47], v[16:19], v[108:111], a[32:47]
	ds_read_b128 v[16:19], v84 offset:3072
	v_mfma_f32_32x32x16_f16 a[16:31], v[20:23], v[108:111], a[16:31]
	ds_read_b128 v[20:23], v84 offset:4096
	v_mfma_f32_32x32x16_f16 a[0:15], v[24:27], v[108:111], a[0:15]
	ds_read_b128 v[24:27], v84 offset:5120
	v_mfma_f32_32x32x16_f16 a[80:95], v[28:31], v[112:115], a[80:95]
	s_add_u32 m0, s46, 0x103c0
	s_add_u32 s40, s40, 0x1800
	s_addc_u32 s41, s41, 0
	global_load_lds_dwordx4 v76, s[40:41]
	ds_read_b128 v[28:31], v84 offset:6144
	v_mfma_f32_32x32x16_f16 a[64:79], v[32:35], v[112:115], a[64:79]
	ds_read_b128 v[32:35], v84 offset:7168
	v_mfma_f32_32x32x16_f16 a[48:63], v[36:39], v[112:115], a[48:63]
	s_add_u32 m0, s47, 0x103c0
	s_add_u32 s42, s42, 0x1800
	s_addc_u32 s43, s43, 0
	global_load_lds_dwordx4 v77, s[42:43]
	ds_read_b128 v[36:39], v84 offset:8192
	v_mfma_f32_32x32x16_f16 a[32:47], v[40:43], v[112:115], a[32:47]
	ds_read_b128 v[40:43], v84 offset:9216
	v_mfma_f32_32x32x16_f16 a[16:31], v[44:47], v[112:115], a[16:31]
	s_add_u32 m0, s48, 0x103c0
	s_add_u32 s44, s44, 0x1800
	s_addc_u32 s45, s45, 0
	global_load_lds_dwordx4 v78, s[44:45]
	ds_read_b128 v[44:47], v84 offset:10240
	v_mfma_f32_32x32x16_f16 a[0:15], v[48:51], v[112:115], a[0:15]
	ds_read_b128 v[48:51], v84 offset:11264
	s_waitcnt lgkmcnt(6)
	v_mfma_f32_32x32x16_f16 a[80:95], v[4:7], v[52:55], a[80:95]
	s_waitcnt vmcnt(24)
	ds_write_b128 v81, v[148:151]
	ds_write_b128 v81, v[152:155] offset:1024
	v_mfma_f32_32x32x16_f16 a[64:79], v[8:11], v[52:55], a[64:79]
	ds_write_b128 v81, v[156:159] offset:2048
	ds_write_b128 v81, v[72:75] offset:3072
	v_mfma_f32_32x32x16_f16 a[48:63], v[12:15], v[52:55], a[48:63]
	ds_read_b128 v[100:103], v95
	ds_read_b128 v[104:107], v96
	ds_read_b128 v[108:111], v97
	ds_read_b128 v[112:115], v94
	s_waitcnt vmcnt(10)
	s_waitcnt lgkmcnt(8)
	s_barrier
	ds_read_b128 v[4:7], v84 offset:12288
	ds_read_b128 v[8:11], v84 offset:13312
	ds_read_b128 v[12:15], v84 offset:14336
	v_mfma_f32_32x32x16_f16 a[32:47], v[16:19], v[52:55], a[32:47]
	ds_read_b128 v[16:19], v84 offset:15360
	v_mfma_f32_32x32x16_f16 a[16:31], v[20:23], v[52:55], a[16:31]
	ds_read_b128 v[20:23], v84 offset:16384
	v_mfma_f32_32x32x16_f16 a[0:15], v[24:27], v[52:55], a[0:15]
	ds_read_b128 v[24:27], v84 offset:17408
	s_waitcnt lgkmcnt(6)
	v_mfma_f32_32x32x16_f16 a[80:95], v[28:31], v[56:59], a[80:95]
	s_add_u32 m0, s46, 0x0
	s_add_u32 s40, s40, 0x1800
	s_addc_u32 s41, s41, 0
	global_load_lds_dwordx4 v76, s[40:41]
	ds_read_b128 v[28:31], v84 offset:18432
	v_mfma_f32_32x32x16_f16 a[64:79], v[32:35], v[56:59], a[64:79]
	global_load_dwordx4 v[148:151], v64, s[4:5] offset:1024
	global_load_dwordx4 v[152:155], v66, s[4:5] offset:1024
	ds_read_b128 v[32:35], v84 offset:19456
	v_mfma_f32_32x32x16_f16 a[48:63], v[36:39], v[56:59], a[48:63]
	s_add_u32 m0, s47, 0x0
	s_add_u32 s42, s42, 0x1800
	s_addc_u32 s43, s43, 0
	global_load_lds_dwordx4 v77, s[42:43]
	ds_read_b128 v[36:39], v84 offset:20480
	v_mfma_f32_32x32x16_f16 a[32:47], v[40:43], v[56:59], a[32:47]
	global_load_dwordx4 v[156:159], v68, s[4:5] offset:1024
	global_load_dwordx4 v[72:75], v70, s[4:5] offset:1024
	ds_read_b128 v[40:43], v84 offset:21504
	v_mfma_f32_32x32x16_f16 a[16:31], v[44:47], v[56:59], a[16:31]
	s_add_u32 m0, s48, 0x0
	s_add_u32 s44, s44, 0x1800
	s_addc_u32 s45, s45, 0
	global_load_lds_dwordx4 v78, s[44:45]
	ds_read_b128 v[44:47], v84 offset:22528
	v_mfma_f32_32x32x16_f16 a[0:15], v[48:51], v[56:59], a[0:15]
	ds_read_b128 v[48:51], v84 offset:23552
	s_waitcnt lgkmcnt(6)
	v_mfma_f32_32x32x16_f16 a[80:95], v[4:7], v[60:63], a[80:95]
	v_mfma_f32_32x32x16_f16 a[64:79], v[8:11], v[60:63], a[64:79]
	v_mfma_f32_32x32x16_f16 a[48:63], v[12:15], v[60:63], a[48:63]
	s_waitcnt vmcnt(10)
	s_waitcnt lgkmcnt(0)
	s_barrier
	ds_read_b128 v[4:7], v84 offset:54208
	ds_read_b128 v[8:11], v84 offset:55232
	ds_read_b128 v[12:15], v84 offset:56256
	v_mfma_f32_32x32x16_f16 a[32:47], v[16:19], v[60:63], a[32:47]
	ds_read_b128 v[16:19], v84 offset:57280
	v_mfma_f32_32x32x16_f16 a[16:31], v[20:23], v[60:63], a[16:31]
	ds_read_b128 v[20:23], v84 offset:58304
	v_mfma_f32_32x32x16_f16 a[0:15], v[24:27], v[60:63], a[0:15]
	ds_read_b128 v[24:27], v84 offset:59328
	v_mfma_f32_32x32x16_f16 a[80:95], v[28:31], v[0:3], a[80:95]
	s_add_u32 m0, s46, 0x3000
	s_add_u32 s40, s40, 0x1800
	s_addc_u32 s41, s41, 0
	global_load_lds_dwordx4 v76, s[40:41]
	ds_read_b128 v[28:31], v84 offset:60352
	v_mfma_f32_32x32x16_f16 a[64:79], v[32:35], v[0:3], a[64:79]
	ds_read_b128 v[32:35], v84 offset:61376
	v_mfma_f32_32x32x16_f16 a[48:63], v[36:39], v[0:3], a[48:63]
	s_add_u32 m0, s47, 0x3000
	s_add_u32 s42, s42, 0x1800
	s_addc_u32 s43, s43, 0
	global_load_lds_dwordx4 v77, s[42:43]
	ds_read_b128 v[36:39], v84 offset:62400
	v_mfma_f32_32x32x16_f16 a[32:47], v[40:43], v[0:3], a[32:47]
	ds_read_b128 v[40:43], v84 offset:63424
	v_mfma_f32_32x32x16_f16 a[16:31], v[44:47], v[0:3], a[16:31]
	s_add_u32 m0, s48, 0x3000
	s_add_u32 s44, s44, 0x1800
	s_addc_u32 s45, s45, 0
	global_load_lds_dwordx4 v78, s[44:45]
	ds_read_b128 v[44:47], v84 offset:64448
	v_mfma_f32_32x32x16_f16 a[0:15], v[48:51], v[0:3], a[0:15]
	ds_read_b128 v[48:51], v84 offset:65472
	s_waitcnt lgkmcnt(6)
	v_mfma_f32_32x32x16_f16 a[80:95], v[4:7], v[100:103], a[80:95]
	s_waitcnt vmcnt(24)
	ds_write_b128 v81, v[116:119]
	ds_write_b128 v81, v[120:123] offset:1024
	v_mfma_f32_32x32x16_f16 a[64:79], v[8:11], v[100:103], a[64:79]
	ds_write_b128 v81, v[124:127] offset:2048
	ds_write_b128 v81, v[128:131] offset:3072
	v_mfma_f32_32x32x16_f16 a[48:63], v[12:15], v[100:103], a[48:63]
	ds_read_b128 v[52:55], v95
	ds_read_b128 v[56:59], v96
	ds_read_b128 v[60:63], v97
	ds_read_b128 v[0:3], v94
	s_waitcnt vmcnt(10)
	s_waitcnt lgkmcnt(8)
	s_barrier
	ds_read_b128 v[4:7], v98
	ds_read_b128 v[8:11], v98 offset:1024
	ds_read_b128 v[12:15], v98 offset:2048
	v_mfma_f32_32x32x16_f16 a[32:47], v[16:19], v[100:103], a[32:47]
	ds_read_b128 v[16:19], v98 offset:3072
	v_mfma_f32_32x32x16_f16 a[16:31], v[20:23], v[100:103], a[16:31]
	ds_read_b128 v[20:23], v98 offset:4096
	v_mfma_f32_32x32x16_f16 a[0:15], v[24:27], v[100:103], a[0:15]
	ds_read_b128 v[24:27], v98 offset:5120
	s_waitcnt lgkmcnt(6)
	v_mfma_f32_32x32x16_f16 a[80:95], v[28:31], v[104:107], a[80:95]
	s_add_u32 m0, s46, 0xd3c0
	s_add_u32 s40, s40, 0x1800
	s_addc_u32 s41, s41, 0
	global_load_lds_dwordx4 v76, s[40:41]
	ds_read_b128 v[28:31], v98 offset:6144
	v_mfma_f32_32x32x16_f16 a[64:79], v[32:35], v[104:107], a[64:79]
	global_load_dwordx4 v[116:119], v64, s[4:5] offset:1152
	global_load_dwordx4 v[120:123], v66, s[4:5] offset:1152
	ds_read_b128 v[32:35], v98 offset:7168
	v_mfma_f32_32x32x16_f16 a[48:63], v[36:39], v[104:107], a[48:63]
	s_add_u32 m0, s47, 0xd3c0
	s_add_u32 s42, s42, 0x1800
	s_addc_u32 s43, s43, 0
	global_load_lds_dwordx4 v77, s[42:43]
	ds_read_b128 v[36:39], v98 offset:8192
	v_mfma_f32_32x32x16_f16 a[32:47], v[40:43], v[104:107], a[32:47]
	global_load_dwordx4 v[124:127], v68, s[4:5] offset:1152
	global_load_dwordx4 v[128:131], v70, s[4:5] offset:1152
	ds_read_b128 v[40:43], v98 offset:9216
	v_mfma_f32_32x32x16_f16 a[16:31], v[44:47], v[104:107], a[16:31]
	s_add_u32 m0, s48, 0xd3c0
	s_add_u32 s44, s44, 0x1800
	s_addc_u32 s45, s45, 0
	global_load_lds_dwordx4 v78, s[44:45]
	ds_read_b128 v[44:47], v98 offset:10240
	v_mfma_f32_32x32x16_f16 a[0:15], v[48:51], v[104:107], a[0:15]
	ds_read_b128 v[48:51], v98 offset:11264
	s_waitcnt lgkmcnt(6)
	v_mfma_f32_32x32x16_f16 a[80:95], v[4:7], v[108:111], a[80:95]
	v_mfma_f32_32x32x16_f16 a[64:79], v[8:11], v[108:111], a[64:79]
	v_mfma_f32_32x32x16_f16 a[48:63], v[12:15], v[108:111], a[48:63]
	s_waitcnt vmcnt(10)
	s_waitcnt lgkmcnt(0)
	s_barrier
	ds_read_b128 v[4:7], v84 offset:0
	ds_read_b128 v[8:11], v84 offset:1024
	ds_read_b128 v[12:15], v84 offset:2048
	v_mfma_f32_32x32x16_f16 a[32:47], v[16:19], v[108:111], a[32:47]
	ds_read_b128 v[16:19], v84 offset:3072
	v_mfma_f32_32x32x16_f16 a[16:31], v[20:23], v[108:111], a[16:31]
	ds_read_b128 v[20:23], v84 offset:4096
	v_mfma_f32_32x32x16_f16 a[0:15], v[24:27], v[108:111], a[0:15]
	ds_read_b128 v[24:27], v84 offset:5120
	v_mfma_f32_32x32x16_f16 a[80:95], v[28:31], v[112:115], a[80:95]
	s_add_u32 m0, s46, 0x103c0
	s_add_u32 s40, s40, 0x1800
	s_addc_u32 s41, s41, 0
	global_load_lds_dwordx4 v76, s[40:41]
	ds_read_b128 v[28:31], v84 offset:6144
	v_mfma_f32_32x32x16_f16 a[64:79], v[32:35], v[112:115], a[64:79]
	ds_read_b128 v[32:35], v84 offset:7168
	v_mfma_f32_32x32x16_f16 a[48:63], v[36:39], v[112:115], a[48:63]
	s_add_u32 m0, s47, 0x103c0
	s_add_u32 s42, s42, 0x1800
	s_addc_u32 s43, s43, 0
	global_load_lds_dwordx4 v77, s[42:43]
	ds_read_b128 v[36:39], v84 offset:8192
	v_mfma_f32_32x32x16_f16 a[32:47], v[40:43], v[112:115], a[32:47]
	ds_read_b128 v[40:43], v84 offset:9216
	v_mfma_f32_32x32x16_f16 a[16:31], v[44:47], v[112:115], a[16:31]
	s_add_u32 m0, s48, 0x103c0
	s_add_u32 s44, s44, 0x1800
	s_addc_u32 s45, s45, 0
	global_load_lds_dwordx4 v78, s[44:45]
	ds_read_b128 v[44:47], v84 offset:10240
	v_mfma_f32_32x32x16_f16 a[0:15], v[48:51], v[112:115], a[0:15]
	ds_read_b128 v[48:51], v84 offset:11264
	s_waitcnt lgkmcnt(6)
	v_mfma_f32_32x32x16_f16 a[80:95], v[4:7], v[52:55], a[80:95]
	s_waitcnt vmcnt(24)
	ds_write_b128 v81, v[132:135]
	ds_write_b128 v81, v[136:139] offset:1024
	v_mfma_f32_32x32x16_f16 a[64:79], v[8:11], v[52:55], a[64:79]
	ds_write_b128 v81, v[140:143] offset:2048
	ds_write_b128 v81, v[144:147] offset:3072
	v_mfma_f32_32x32x16_f16 a[48:63], v[12:15], v[52:55], a[48:63]
	ds_read_b128 v[100:103], v95
	ds_read_b128 v[104:107], v96
	ds_read_b128 v[108:111], v97
	ds_read_b128 v[112:115], v94
	s_waitcnt vmcnt(10)
	s_waitcnt lgkmcnt(8)
	s_barrier
	ds_read_b128 v[4:7], v84 offset:12288
	ds_read_b128 v[8:11], v84 offset:13312
	ds_read_b128 v[12:15], v84 offset:14336
	v_mfma_f32_32x32x16_f16 a[32:47], v[16:19], v[52:55], a[32:47]
	ds_read_b128 v[16:19], v84 offset:15360
	v_mfma_f32_32x32x16_f16 a[16:31], v[20:23], v[52:55], a[16:31]
	ds_read_b128 v[20:23], v84 offset:16384
	v_mfma_f32_32x32x16_f16 a[0:15], v[24:27], v[52:55], a[0:15]
	ds_read_b128 v[24:27], v84 offset:17408
	s_waitcnt lgkmcnt(6)
	v_mfma_f32_32x32x16_f16 a[80:95], v[28:31], v[56:59], a[80:95]
	s_add_u32 m0, s46, 0x0
	s_add_u32 s40, s40, 0x1800
	s_addc_u32 s41, s41, 0
	global_load_lds_dwordx4 v76, s[40:41]
	ds_read_b128 v[28:31], v84 offset:18432
	v_mfma_f32_32x32x16_f16 a[64:79], v[32:35], v[56:59], a[64:79]
	global_load_dwordx4 v[132:135], v64, s[4:5] offset:1280
	global_load_dwordx4 v[136:139], v66, s[4:5] offset:1280
	ds_read_b128 v[32:35], v84 offset:19456
	v_mfma_f32_32x32x16_f16 a[48:63], v[36:39], v[56:59], a[48:63]
	s_add_u32 m0, s47, 0x0
	s_add_u32 s42, s42, 0x1800
	s_addc_u32 s43, s43, 0
	global_load_lds_dwordx4 v77, s[42:43]
	ds_read_b128 v[36:39], v84 offset:20480
	v_mfma_f32_32x32x16_f16 a[32:47], v[40:43], v[56:59], a[32:47]
	global_load_dwordx4 v[140:143], v68, s[4:5] offset:1280
	global_load_dwordx4 v[144:147], v70, s[4:5] offset:1280
	ds_read_b128 v[40:43], v84 offset:21504
	v_mfma_f32_32x32x16_f16 a[16:31], v[44:47], v[56:59], a[16:31]
	s_add_u32 m0, s48, 0x0
	s_add_u32 s44, s44, 0x1800
	s_addc_u32 s45, s45, 0
	global_load_lds_dwordx4 v78, s[44:45]
	ds_read_b128 v[44:47], v84 offset:22528
	v_mfma_f32_32x32x16_f16 a[0:15], v[48:51], v[56:59], a[0:15]
	ds_read_b128 v[48:51], v84 offset:23552
	s_waitcnt lgkmcnt(6)
	v_mfma_f32_32x32x16_f16 a[80:95], v[4:7], v[60:63], a[80:95]
	v_mfma_f32_32x32x16_f16 a[64:79], v[8:11], v[60:63], a[64:79]
	v_mfma_f32_32x32x16_f16 a[48:63], v[12:15], v[60:63], a[48:63]
	s_waitcnt vmcnt(10)
	s_waitcnt lgkmcnt(0)
	s_barrier
	ds_read_b128 v[4:7], v84 offset:54208
	ds_read_b128 v[8:11], v84 offset:55232
	ds_read_b128 v[12:15], v84 offset:56256
	v_mfma_f32_32x32x16_f16 a[32:47], v[16:19], v[60:63], a[32:47]
	ds_read_b128 v[16:19], v84 offset:57280
	v_mfma_f32_32x32x16_f16 a[16:31], v[20:23], v[60:63], a[16:31]
	ds_read_b128 v[20:23], v84 offset:58304
	v_mfma_f32_32x32x16_f16 a[0:15], v[24:27], v[60:63], a[0:15]
	ds_read_b128 v[24:27], v84 offset:59328
	v_mfma_f32_32x32x16_f16 a[80:95], v[28:31], v[0:3], a[80:95]
	s_add_u32 m0, s46, 0x3000
	s_add_u32 s40, s40, 0x1800
	s_addc_u32 s41, s41, 0
	global_load_lds_dwordx4 v76, s[40:41]
	ds_read_b128 v[28:31], v84 offset:60352
	v_mfma_f32_32x32x16_f16 a[64:79], v[32:35], v[0:3], a[64:79]
	ds_read_b128 v[32:35], v84 offset:61376
	v_mfma_f32_32x32x16_f16 a[48:63], v[36:39], v[0:3], a[48:63]
	s_add_u32 m0, s47, 0x3000
	s_add_u32 s42, s42, 0x1800
	s_addc_u32 s43, s43, 0
	global_load_lds_dwordx4 v77, s[42:43]
	ds_read_b128 v[36:39], v84 offset:62400
	v_mfma_f32_32x32x16_f16 a[32:47], v[40:43], v[0:3], a[32:47]
	ds_read_b128 v[40:43], v84 offset:63424
	v_mfma_f32_32x32x16_f16 a[16:31], v[44:47], v[0:3], a[16:31]
	s_add_u32 m0, s48, 0x3000
	s_add_u32 s44, s44, 0x1800
	s_addc_u32 s45, s45, 0
	global_load_lds_dwordx4 v78, s[44:45]
	ds_read_b128 v[44:47], v84 offset:64448
	v_mfma_f32_32x32x16_f16 a[0:15], v[48:51], v[0:3], a[0:15]
	ds_read_b128 v[48:51], v84 offset:65472
	s_waitcnt lgkmcnt(6)
	v_mfma_f32_32x32x16_f16 a[80:95], v[4:7], v[100:103], a[80:95]
	s_waitcnt vmcnt(24)
	ds_write_b128 v81, v[148:151]
	ds_write_b128 v81, v[152:155] offset:1024
	v_mfma_f32_32x32x16_f16 a[64:79], v[8:11], v[100:103], a[64:79]
	ds_write_b128 v81, v[156:159] offset:2048
	ds_write_b128 v81, v[72:75] offset:3072
	v_mfma_f32_32x32x16_f16 a[48:63], v[12:15], v[100:103], a[48:63]
	ds_read_b128 v[52:55], v95
	ds_read_b128 v[56:59], v96
	ds_read_b128 v[60:63], v97
	ds_read_b128 v[0:3], v94
	s_waitcnt vmcnt(10)
	s_waitcnt lgkmcnt(8)
	s_barrier
	ds_read_b128 v[4:7], v98
	ds_read_b128 v[8:11], v98 offset:1024
	ds_read_b128 v[12:15], v98 offset:2048
	v_mfma_f32_32x32x16_f16 a[32:47], v[16:19], v[100:103], a[32:47]
	ds_read_b128 v[16:19], v98 offset:3072
	v_mfma_f32_32x32x16_f16 a[16:31], v[20:23], v[100:103], a[16:31]
	ds_read_b128 v[20:23], v98 offset:4096
	v_mfma_f32_32x32x16_f16 a[0:15], v[24:27], v[100:103], a[0:15]
	ds_read_b128 v[24:27], v98 offset:5120
	s_waitcnt lgkmcnt(6)
	v_mfma_f32_32x32x16_f16 a[80:95], v[28:31], v[104:107], a[80:95]
	s_add_u32 m0, s46, 0xd3c0
	s_add_u32 s40, s40, 0x1800
	s_addc_u32 s41, s41, 0
	global_load_lds_dwordx4 v76, s[40:41]
	ds_read_b128 v[28:31], v98 offset:6144
	v_mfma_f32_32x32x16_f16 a[64:79], v[32:35], v[104:107], a[64:79]
	global_load_dwordx4 v[148:151], v64, s[4:5] offset:1408
	global_load_dwordx4 v[152:155], v66, s[4:5] offset:1408
	ds_read_b128 v[32:35], v98 offset:7168
	v_mfma_f32_32x32x16_f16 a[48:63], v[36:39], v[104:107], a[48:63]
	s_add_u32 m0, s47, 0xd3c0
	s_add_u32 s42, s42, 0x1800
	s_addc_u32 s43, s43, 0
	global_load_lds_dwordx4 v77, s[42:43]
	ds_read_b128 v[36:39], v98 offset:8192
	v_mfma_f32_32x32x16_f16 a[32:47], v[40:43], v[104:107], a[32:47]
	global_load_dwordx4 v[156:159], v68, s[4:5] offset:1408
	global_load_dwordx4 v[72:75], v70, s[4:5] offset:1408
	ds_read_b128 v[40:43], v98 offset:9216
	v_mfma_f32_32x32x16_f16 a[16:31], v[44:47], v[104:107], a[16:31]
	s_add_u32 m0, s48, 0xd3c0
	s_add_u32 s44, s44, 0x1800
	s_addc_u32 s45, s45, 0
	global_load_lds_dwordx4 v78, s[44:45]
	ds_read_b128 v[44:47], v98 offset:10240
	v_mfma_f32_32x32x16_f16 a[0:15], v[48:51], v[104:107], a[0:15]
	ds_read_b128 v[48:51], v98 offset:11264
	s_waitcnt lgkmcnt(6)
	v_mfma_f32_32x32x16_f16 a[80:95], v[4:7], v[108:111], a[80:95]
	v_mfma_f32_32x32x16_f16 a[64:79], v[8:11], v[108:111], a[64:79]
	v_mfma_f32_32x32x16_f16 a[48:63], v[12:15], v[108:111], a[48:63]
	s_waitcnt vmcnt(10)
	s_waitcnt lgkmcnt(0)
	s_barrier
	ds_read_b128 v[4:7], v84 offset:0
	ds_read_b128 v[8:11], v84 offset:1024
	ds_read_b128 v[12:15], v84 offset:2048
	v_mfma_f32_32x32x16_f16 a[32:47], v[16:19], v[108:111], a[32:47]
	ds_read_b128 v[16:19], v84 offset:3072
	v_mfma_f32_32x32x16_f16 a[16:31], v[20:23], v[108:111], a[16:31]
	ds_read_b128 v[20:23], v84 offset:4096
	v_mfma_f32_32x32x16_f16 a[0:15], v[24:27], v[108:111], a[0:15]
	ds_read_b128 v[24:27], v84 offset:5120
	v_mfma_f32_32x32x16_f16 a[80:95], v[28:31], v[112:115], a[80:95]
	s_add_u32 m0, s46, 0x103c0
	s_add_u32 s40, s40, 0x1800
	s_addc_u32 s41, s41, 0
	global_load_lds_dwordx4 v76, s[40:41]
	ds_read_b128 v[28:31], v84 offset:6144
	v_mfma_f32_32x32x16_f16 a[64:79], v[32:35], v[112:115], a[64:79]
	ds_read_b128 v[32:35], v84 offset:7168
	v_mfma_f32_32x32x16_f16 a[48:63], v[36:39], v[112:115], a[48:63]
	s_add_u32 m0, s47, 0x103c0
	s_add_u32 s42, s42, 0x1800
	s_addc_u32 s43, s43, 0
	global_load_lds_dwordx4 v77, s[42:43]
	ds_read_b128 v[36:39], v84 offset:8192
	v_mfma_f32_32x32x16_f16 a[32:47], v[40:43], v[112:115], a[32:47]
	ds_read_b128 v[40:43], v84 offset:9216
	v_mfma_f32_32x32x16_f16 a[16:31], v[44:47], v[112:115], a[16:31]
	s_add_u32 m0, s48, 0x103c0
	s_add_u32 s44, s44, 0x1800
	s_addc_u32 s45, s45, 0
	global_load_lds_dwordx4 v78, s[44:45]
	ds_read_b128 v[44:47], v84 offset:10240
	v_mfma_f32_32x32x16_f16 a[0:15], v[48:51], v[112:115], a[0:15]
	ds_read_b128 v[48:51], v84 offset:11264
	s_waitcnt lgkmcnt(6)
	v_mfma_f32_32x32x16_f16 a[80:95], v[4:7], v[52:55], a[80:95]
	s_waitcnt vmcnt(24)
	ds_write_b128 v81, v[116:119]
	ds_write_b128 v81, v[120:123] offset:1024
	v_mfma_f32_32x32x16_f16 a[64:79], v[8:11], v[52:55], a[64:79]
	ds_write_b128 v81, v[124:127] offset:2048
	ds_write_b128 v81, v[128:131] offset:3072
	v_mfma_f32_32x32x16_f16 a[48:63], v[12:15], v[52:55], a[48:63]
	ds_read_b128 v[100:103], v95
	ds_read_b128 v[104:107], v96
	ds_read_b128 v[108:111], v97
	ds_read_b128 v[112:115], v94
	s_waitcnt vmcnt(10)
	s_waitcnt lgkmcnt(8)
	s_barrier
	ds_read_b128 v[4:7], v84 offset:12288
	ds_read_b128 v[8:11], v84 offset:13312
	ds_read_b128 v[12:15], v84 offset:14336
	v_mfma_f32_32x32x16_f16 a[32:47], v[16:19], v[52:55], a[32:47]
	ds_read_b128 v[16:19], v84 offset:15360
	v_mfma_f32_32x32x16_f16 a[16:31], v[20:23], v[52:55], a[16:31]
	ds_read_b128 v[20:23], v84 offset:16384
	v_mfma_f32_32x32x16_f16 a[0:15], v[24:27], v[52:55], a[0:15]
	ds_read_b128 v[24:27], v84 offset:17408
	s_waitcnt lgkmcnt(6)
	v_mfma_f32_32x32x16_f16 a[80:95], v[28:31], v[56:59], a[80:95]
	s_add_u32 m0, s46, 0x0
	s_add_u32 s40, s40, 0x1800
	s_addc_u32 s41, s41, 0
	global_load_lds_dwordx4 v76, s[40:41]
	ds_read_b128 v[28:31], v84 offset:18432
	v_mfma_f32_32x32x16_f16 a[64:79], v[32:35], v[56:59], a[64:79]
	global_load_dwordx4 v[116:119], v64, s[4:5] offset:1440
	global_load_dwordx4 v[120:123], v66, s[4:5] offset:1440
	ds_read_b128 v[32:35], v84 offset:19456
	v_mfma_f32_32x32x16_f16 a[48:63], v[36:39], v[56:59], a[48:63]
	s_add_u32 m0, s47, 0x0
	s_add_u32 s42, s42, 0x1800
	s_addc_u32 s43, s43, 0
	global_load_lds_dwordx4 v77, s[42:43]
	ds_read_b128 v[36:39], v84 offset:20480
	v_mfma_f32_32x32x16_f16 a[32:47], v[40:43], v[56:59], a[32:47]
	global_load_dwordx4 v[124:127], v68, s[4:5] offset:1440
	global_load_dwordx4 v[128:131], v70, s[4:5] offset:1440
	ds_read_b128 v[40:43], v84 offset:21504
	v_mfma_f32_32x32x16_f16 a[16:31], v[44:47], v[56:59], a[16:31]
	s_add_u32 m0, s48, 0x0
	s_add_u32 s44, s44, 0x1800
	s_addc_u32 s45, s45, 0
	global_load_lds_dwordx4 v78, s[44:45]
	ds_read_b128 v[44:47], v84 offset:22528
	v_mfma_f32_32x32x16_f16 a[0:15], v[48:51], v[56:59], a[0:15]
	ds_read_b128 v[48:51], v84 offset:23552
	s_waitcnt lgkmcnt(6)
	v_mfma_f32_32x32x16_f16 a[80:95], v[4:7], v[60:63], a[80:95]
	v_mfma_f32_32x32x16_f16 a[64:79], v[8:11], v[60:63], a[64:79]
	v_mfma_f32_32x32x16_f16 a[48:63], v[12:15], v[60:63], a[48:63]
	s_waitcnt vmcnt(10)
	s_waitcnt lgkmcnt(0)
	s_barrier
	ds_read_b128 v[4:7], v84 offset:54208
	ds_read_b128 v[8:11], v84 offset:55232
	ds_read_b128 v[12:15], v84 offset:56256
	v_mfma_f32_32x32x16_f16 a[32:47], v[16:19], v[60:63], a[32:47]
	ds_read_b128 v[16:19], v84 offset:57280
	v_mfma_f32_32x32x16_f16 a[16:31], v[20:23], v[60:63], a[16:31]
	ds_read_b128 v[20:23], v84 offset:58304
	v_mfma_f32_32x32x16_f16 a[0:15], v[24:27], v[60:63], a[0:15]
	ds_read_b128 v[24:27], v84 offset:59328
	v_mfma_f32_32x32x16_f16 a[80:95], v[28:31], v[0:3], a[80:95]
	s_add_u32 m0, s46, 0x3000
	s_add_u32 s40, s40, 0x1800
	s_addc_u32 s41, s41, 0
	global_load_lds_dwordx4 v76, s[40:41]
	ds_read_b128 v[28:31], v84 offset:60352
	v_mfma_f32_32x32x16_f16 a[64:79], v[32:35], v[0:3], a[64:79]
	ds_read_b128 v[32:35], v84 offset:61376
	v_mfma_f32_32x32x16_f16 a[48:63], v[36:39], v[0:3], a[48:63]
	s_add_u32 m0, s47, 0x3000
	s_add_u32 s42, s42, 0x1800
	s_addc_u32 s43, s43, 0
	global_load_lds_dwordx4 v77, s[42:43]
	ds_read_b128 v[36:39], v84 offset:62400
	v_mfma_f32_32x32x16_f16 a[32:47], v[40:43], v[0:3], a[32:47]
	ds_read_b128 v[40:43], v84 offset:63424
	v_mfma_f32_32x32x16_f16 a[16:31], v[44:47], v[0:3], a[16:31]
	s_add_u32 m0, s48, 0x3000
	s_add_u32 s44, s44, 0x1800
	s_addc_u32 s45, s45, 0
	global_load_lds_dwordx4 v78, s[44:45]
	ds_read_b128 v[44:47], v84 offset:64448
	v_mfma_f32_32x32x16_f16 a[0:15], v[48:51], v[0:3], a[0:15]
	ds_read_b128 v[48:51], v84 offset:65472
	s_waitcnt lgkmcnt(6)
	v_mfma_f32_32x32x16_f16 a[80:95], v[4:7], v[100:103], a[80:95]
	s_waitcnt vmcnt(24)
	ds_write_b128 v81, v[132:135]
	ds_write_b128 v81, v[136:139] offset:1024
	v_mfma_f32_32x32x16_f16 a[64:79], v[8:11], v[100:103], a[64:79]
	ds_write_b128 v81, v[140:143] offset:2048
	ds_write_b128 v81, v[144:147] offset:3072
	v_mfma_f32_32x32x16_f16 a[48:63], v[12:15], v[100:103], a[48:63]
	ds_read_b128 v[52:55], v95
	ds_read_b128 v[56:59], v96
	ds_read_b128 v[60:63], v97
	ds_read_b128 v[0:3], v94
	s_waitcnt vmcnt(10)
	s_waitcnt lgkmcnt(8)
	s_barrier
	ds_read_b128 v[4:7], v98
	ds_read_b128 v[8:11], v98 offset:1024
	ds_read_b128 v[12:15], v98 offset:2048
	v_mfma_f32_32x32x16_f16 a[32:47], v[16:19], v[100:103], a[32:47]
	ds_read_b128 v[16:19], v98 offset:3072
	v_mfma_f32_32x32x16_f16 a[16:31], v[20:23], v[100:103], a[16:31]
	ds_read_b128 v[20:23], v98 offset:4096
	v_mfma_f32_32x32x16_f16 a[0:15], v[24:27], v[100:103], a[0:15]
	ds_read_b128 v[24:27], v98 offset:5120
	s_waitcnt lgkmcnt(6)
	v_mfma_f32_32x32x16_f16 a[80:95], v[28:31], v[104:107], a[80:95]
	s_add_u32 m0, s46, 0xd3c0
	s_add_u32 s40, s40, 0x1800
	s_addc_u32 s41, s41, 0
	global_load_lds_dwordx4 v76, s[40:41]
	ds_read_b128 v[28:31], v98 offset:6144
	v_mfma_f32_32x32x16_f16 a[64:79], v[32:35], v[104:107], a[64:79]
	ds_read_b128 v[32:35], v98 offset:7168
	v_mfma_f32_32x32x16_f16 a[48:63], v[36:39], v[104:107], a[48:63]
	s_add_u32 m0, s47, 0xd3c0
	s_add_u32 s42, s42, 0x1800
	s_addc_u32 s43, s43, 0
	global_load_lds_dwordx4 v77, s[42:43]
	ds_read_b128 v[36:39], v98 offset:8192
	v_mfma_f32_32x32x16_f16 a[32:47], v[40:43], v[104:107], a[32:47]
	ds_read_b128 v[40:43], v98 offset:9216
	v_mfma_f32_32x32x16_f16 a[16:31], v[44:47], v[104:107], a[16:31]
	s_add_u32 m0, s48, 0xd3c0
	s_add_u32 s44, s44, 0x1800
	s_addc_u32 s45, s45, 0
	global_load_lds_dwordx4 v78, s[44:45]
	ds_read_b128 v[44:47], v98 offset:10240
	v_mfma_f32_32x32x16_f16 a[0:15], v[48:51], v[104:107], a[0:15]
	ds_read_b128 v[48:51], v98 offset:11264
	s_waitcnt lgkmcnt(6)
	v_mfma_f32_32x32x16_f16 a[80:95], v[4:7], v[108:111], a[80:95]
	v_mfma_f32_32x32x16_f16 a[64:79], v[8:11], v[108:111], a[64:79]
	v_mfma_f32_32x32x16_f16 a[48:63], v[12:15], v[108:111], a[48:63]
	s_waitcnt vmcnt(6)
	s_waitcnt lgkmcnt(0)
	s_barrier
	ds_read_b128 v[4:7], v84 offset:0
	ds_read_b128 v[8:11], v84 offset:1024
	ds_read_b128 v[12:15], v84 offset:2048
	v_mfma_f32_32x32x16_f16 a[32:47], v[16:19], v[108:111], a[32:47]
	ds_read_b128 v[16:19], v84 offset:3072
	v_mfma_f32_32x32x16_f16 a[16:31], v[20:23], v[108:111], a[16:31]
	ds_read_b128 v[20:23], v84 offset:4096
	v_mfma_f32_32x32x16_f16 a[0:15], v[24:27], v[108:111], a[0:15]
	ds_read_b128 v[24:27], v84 offset:5120
	v_mfma_f32_32x32x16_f16 a[80:95], v[28:31], v[112:115], a[80:95]
	s_add_u32 m0, s46, 0x103c0
	s_add_u32 s40, s40, 0x1800
	s_addc_u32 s41, s41, 0
	global_load_lds_dwordx4 v76, s[40:41]
	ds_read_b128 v[28:31], v84 offset:6144
	v_mfma_f32_32x32x16_f16 a[64:79], v[32:35], v[112:115], a[64:79]
	ds_read_b128 v[32:35], v84 offset:7168
	v_mfma_f32_32x32x16_f16 a[48:63], v[36:39], v[112:115], a[48:63]
	s_add_u32 m0, s47, 0x103c0
	s_add_u32 s42, s42, 0x1800
	s_addc_u32 s43, s43, 0
	global_load_lds_dwordx4 v77, s[42:43]
	ds_read_b128 v[36:39], v84 offset:8192
	v_mfma_f32_32x32x16_f16 a[32:47], v[40:43], v[112:115], a[32:47]
	ds_read_b128 v[40:43], v84 offset:9216
	v_mfma_f32_32x32x16_f16 a[16:31], v[44:47], v[112:115], a[16:31]
	s_add_u32 m0, s48, 0x103c0
	s_add_u32 s44, s44, 0x1800
	s_addc_u32 s45, s45, 0
	global_load_lds_dwordx4 v78, s[44:45]
	ds_read_b128 v[44:47], v84 offset:10240
	v_mfma_f32_32x32x16_f16 a[0:15], v[48:51], v[112:115], a[0:15]
	ds_read_b128 v[48:51], v84 offset:11264
	s_waitcnt lgkmcnt(6)
	v_mfma_f32_32x32x16_f16 a[80:95], v[4:7], v[52:55], a[80:95]
	s_waitcnt vmcnt(20)
	ds_write_b128 v81, v[148:151]
	ds_write_b128 v81, v[152:155] offset:1024
	v_mfma_f32_32x32x16_f16 a[64:79], v[8:11], v[52:55], a[64:79]
	ds_write_b128 v81, v[156:159] offset:2048
	ds_write_b128 v81, v[72:75] offset:3072
	v_mfma_f32_32x32x16_f16 a[48:63], v[12:15], v[52:55], a[48:63]
	ds_read_b128 v[100:103], v95
	ds_read_b128 v[104:107], v96
	ds_read_b128 v[108:111], v97
	ds_read_b128 v[112:115], v94
	s_waitcnt vmcnt(6)
	s_waitcnt lgkmcnt(8)
	s_barrier
	ds_read_b128 v[4:7], v84 offset:12288
	ds_read_b128 v[8:11], v84 offset:13312
	ds_read_b128 v[12:15], v84 offset:14336
	v_mfma_f32_32x32x16_f16 a[32:47], v[16:19], v[52:55], a[32:47]
	ds_read_b128 v[16:19], v84 offset:15360
	v_mfma_f32_32x32x16_f16 a[16:31], v[20:23], v[52:55], a[16:31]
	ds_read_b128 v[20:23], v84 offset:16384
	v_mfma_f32_32x32x16_f16 a[0:15], v[24:27], v[52:55], a[0:15]
	ds_read_b128 v[24:27], v84 offset:17408
	s_waitcnt lgkmcnt(6)
	v_mfma_f32_32x32x16_f16 a[80:95], v[28:31], v[56:59], a[80:95]
	s_add_u32 m0, s46, 0x0
	s_add_u32 s40, s40, 0x1800
	s_addc_u32 s41, s41, 0
	global_load_lds_dwordx4 v76, s[40:41]
	ds_read_b128 v[28:31], v84 offset:18432
	v_mfma_f32_32x32x16_f16 a[64:79], v[32:35], v[56:59], a[64:79]
	ds_read_b128 v[32:35], v84 offset:19456
	v_mfma_f32_32x32x16_f16 a[48:63], v[36:39], v[56:59], a[48:63]
	s_add_u32 m0, s47, 0x0
	s_add_u32 s42, s42, s49
	s_addc_u32 s43, s43, 0
	global_load_lds_dwordx4 v77, s[42:43]
	ds_read_b128 v[36:39], v84 offset:20480
	v_mfma_f32_32x32x16_f16 a[32:47], v[40:43], v[56:59], a[32:47]
	ds_read_b128 v[40:43], v84 offset:21504
	v_mfma_f32_32x32x16_f16 a[16:31], v[44:47], v[56:59], a[16:31]
	s_add_u32 m0, s48, 0x0
	s_add_u32 s44, s44, 0xc00
	s_addc_u32 s45, s45, 0
	global_load_lds_dwordx4 v78, s[44:45]
	ds_read_b128 v[44:47], v84 offset:22528
	v_mfma_f32_32x32x16_f16 a[0:15], v[48:51], v[56:59], a[0:15]
	ds_read_b128 v[48:51], v84 offset:23552
	s_waitcnt lgkmcnt(6)
	v_mfma_f32_32x32x16_f16 a[80:95], v[4:7], v[60:63], a[80:95]
	v_mfma_f32_32x32x16_f16 a[64:79], v[8:11], v[60:63], a[64:79]
	v_mfma_f32_32x32x16_f16 a[48:63], v[12:15], v[60:63], a[48:63]
	s_waitcnt vmcnt(6)
	s_waitcnt lgkmcnt(0)
	s_barrier
	ds_read_b128 v[4:7], v84 offset:54208
	ds_read_b128 v[8:11], v84 offset:55232
	ds_read_b128 v[12:15], v84 offset:56256
	v_mfma_f32_32x32x16_f16 a[32:47], v[16:19], v[60:63], a[32:47]
	ds_read_b128 v[16:19], v84 offset:57280
	v_mfma_f32_32x32x16_f16 a[16:31], v[20:23], v[60:63], a[16:31]
	ds_read_b128 v[20:23], v84 offset:58304
	v_mfma_f32_32x32x16_f16 a[0:15], v[24:27], v[60:63], a[0:15]
	ds_read_b128 v[24:27], v84 offset:59328
	v_mfma_f32_32x32x16_f16 a[80:95], v[28:31], v[0:3], a[80:95]
	ds_read_b128 v[28:31], v84 offset:60352
	v_mfma_f32_32x32x16_f16 a[64:79], v[32:35], v[0:3], a[64:79]
	ds_read_b128 v[32:35], v84 offset:61376
	v_mfma_f32_32x32x16_f16 a[48:63], v[36:39], v[0:3], a[48:63]
	ds_read_b128 v[36:39], v84 offset:62400
	v_mfma_f32_32x32x16_f16 a[32:47], v[40:43], v[0:3], a[32:47]
	ds_read_b128 v[40:43], v84 offset:63424
	v_mfma_f32_32x32x16_f16 a[16:31], v[44:47], v[0:3], a[16:31]
	ds_read_b128 v[44:47], v84 offset:64448
	v_mfma_f32_32x32x16_f16 a[0:15], v[48:51], v[0:3], a[0:15]
	ds_read_b128 v[48:51], v84 offset:65472
	s_waitcnt lgkmcnt(6)
	v_mfma_f32_32x32x16_f16 a[80:95], v[4:7], v[100:103], a[80:95]
	s_waitcnt vmcnt(13)
	ds_write_b128 v81, v[116:119]
	ds_write_b128 v81, v[120:123] offset:1024
	v_mfma_f32_32x32x16_f16 a[64:79], v[8:11], v[100:103], a[64:79]
	ds_write_b128 v81, v[124:127] offset:2048
	ds_write_b128 v81, v[128:131] offset:3072
	v_mfma_f32_32x32x16_f16 a[48:63], v[12:15], v[100:103], a[48:63]
	ds_read_b128 v[0:3], v94
	s_waitcnt vmcnt(3)
	s_waitcnt lgkmcnt(5)
	s_barrier
	ds_read_b128 v[4:7], v98
	ds_read_b128 v[8:11], v98 offset:1024
	ds_read_b128 v[12:15], v98 offset:2048
	v_mfma_f32_32x32x16_f16 a[32:47], v[16:19], v[100:103], a[32:47]
	ds_read_b128 v[16:19], v98 offset:3072
	v_mfma_f32_32x32x16_f16 a[16:31], v[20:23], v[100:103], a[16:31]
	ds_read_b128 v[20:23], v98 offset:4096
	v_mfma_f32_32x32x16_f16 a[0:15], v[24:27], v[100:103], a[0:15]
	ds_read_b128 v[24:27], v98 offset:5120
	s_waitcnt lgkmcnt(6)
	v_mfma_f32_32x32x16_f16 a[80:95], v[28:31], v[104:107], a[80:95]
	ds_read_b128 v[28:31], v98 offset:6144
	v_mfma_f32_32x32x16_f16 a[64:79], v[32:35], v[104:107], a[64:79]
	ds_read_b128 v[32:35], v98 offset:7168
	v_mfma_f32_32x32x16_f16 a[48:63], v[36:39], v[104:107], a[48:63]
	ds_read_b128 v[36:39], v98 offset:8192
	v_mfma_f32_32x32x16_f16 a[32:47], v[40:43], v[104:107], a[32:47]
	ds_read_b128 v[40:43], v98 offset:9216
	v_mfma_f32_32x32x16_f16 a[16:31], v[44:47], v[104:107], a[16:31]
	ds_read_b128 v[44:47], v98 offset:10240
	v_mfma_f32_32x32x16_f16 a[0:15], v[48:51], v[104:107], a[0:15]
	ds_read_b128 v[48:51], v98 offset:11264
	s_waitcnt lgkmcnt(6)
	v_mfma_f32_32x32x16_f16 a[80:95], v[4:7], v[108:111], a[80:95]
	v_mfma_f32_32x32x16_f16 a[64:79], v[8:11], v[108:111], a[64:79]
	v_mfma_f32_32x32x16_f16 a[48:63], v[12:15], v[108:111], a[48:63]
	s_waitcnt vmcnt(0)
	s_waitcnt lgkmcnt(0)
	s_barrier
	ds_read_b128 v[4:7], v84 offset:0
	ds_read_b128 v[8:11], v84 offset:1024
	ds_read_b128 v[12:15], v84 offset:2048
	v_mfma_f32_32x32x16_f16 a[32:47], v[16:19], v[108:111], a[32:47]
	ds_read_b128 v[16:19], v84 offset:3072
	v_mfma_f32_32x32x16_f16 a[16:31], v[20:23], v[108:111], a[16:31]
	ds_read_b128 v[20:23], v84 offset:4096
	v_mfma_f32_32x32x16_f16 a[0:15], v[24:27], v[108:111], a[0:15]
	ds_read_b128 v[24:27], v84 offset:5120
	v_mfma_f32_32x32x16_f16 a[80:95], v[28:31], v[112:115], a[80:95]
	v_mfma_f32_32x32x16_f16 a[64:79], v[32:35], v[112:115], a[64:79]
	v_mfma_f32_32x32x16_f16 a[48:63], v[36:39], v[112:115], a[48:63]
	v_mfma_f32_32x32x16_f16 a[32:47], v[40:43], v[112:115], a[32:47]
	v_mfma_f32_32x32x16_f16 a[16:31], v[44:47], v[112:115], a[16:31]
	v_mfma_f32_32x32x16_f16 a[0:15], v[48:51], v[112:115], a[0:15]
	s_waitcnt lgkmcnt(0)
	v_mfma_f32_32x32x16_f16 a[80:95], v[4:7], v[0:3], a[80:95]
	v_mfma_f32_32x32x16_f16 a[16:31], v[20:23], v[0:3], a[16:31]
	v_lshlrev_b32_e32 v22, 4, v85
	v_mfma_f32_32x32x16_f16 a[64:79], v[8:11], v[0:3], a[64:79]
	v_mfma_f32_32x32x16_f16 a[48:63], v[12:15], v[0:3], a[48:63]
	s_nop 7
	v_accvgpr_read_b32 v13, a88
	v_mfma_f32_32x32x16_f16 a[32:47], v[16:19], v[0:3], a[32:47]
	v_accvgpr_read_b32 v17, a92
	v_mfma_f32_32x32x16_f16 a[0:15], v[24:27], v[0:3], a[0:15]
	ds_read_b128 v[2:5], v22 offset:53248
	ds_read_b128 v[6:9], v22 offset:53280
	v_accvgpr_read_b32 v1, a80
	v_lshlrev_b32_e32 v0, 4, v92
	s_waitcnt lgkmcnt(1)
	v_add_f32_e32 v1, v1, v2
	v_accvgpr_read_b32 v2, a81
	v_add_f32_e32 v2, v3, v2
	v_max_f32_e32 v10, 0, v2
	v_accvgpr_read_b32 v2, a82
	v_add_f32_e32 v2, v4, v2
	v_max_f32_e32 v11, 0, v2
	v_accvgpr_read_b32 v2, a83
	v_add_f32_e32 v2, v5, v2
	v_max_f32_e32 v12, 0, v2
	v_accvgpr_read_b32 v2, a84
	s_waitcnt lgkmcnt(0)
	v_add_f32_e32 v2, v2, v6
	v_max_f32_e32 v6, 0, v2
	v_accvgpr_read_b32 v2, a85
	v_add_f32_e32 v2, v7, v2
	v_max_f32_e32 v7, 0, v2
	v_accvgpr_read_b32 v2, a86
	v_add_f32_e32 v2, v8, v2
	v_max_f32_e32 v8, 0, v2
	v_accvgpr_read_b32 v2, a87
	v_add_f32_e32 v2, v9, v2
	v_max_f32_e32 v9, 0, v2
	ds_read_b128 v[2:5], v22 offset:53312
	v_max_f32_e32 v1, 0, v1
	s_waitcnt lgkmcnt(0)
	v_add_f32_e32 v2, v13, v2
	v_max_f32_e32 v13, 0, v2
	v_accvgpr_read_b32 v2, a89
	v_add_f32_e32 v2, v3, v2
	v_max_f32_e32 v14, 0, v2
	v_accvgpr_read_b32 v2, a90
	v_add_f32_e32 v2, v4, v2
	v_max_f32_e32 v15, 0, v2
	v_accvgpr_read_b32 v2, a91
	v_add_f32_e32 v2, v5, v2
	v_max_f32_e32 v16, 0, v2
	ds_read_b128 v[2:5], v22 offset:53344
	s_waitcnt lgkmcnt(0)
	v_add_f32_e32 v2, v17, v2
	v_max_f32_e32 v17, 0, v2
	v_accvgpr_read_b32 v2, a93
	v_add_f32_e32 v2, v3, v2
	v_max_f32_e32 v18, 0, v2
	v_accvgpr_read_b32 v2, a94
	v_add_f32_e32 v2, v4, v2
	v_max_f32_e32 v19, 0, v2
	v_accvgpr_read_b32 v2, a95
	v_add_f32_e32 v2, v5, v2
	v_cvt_pk_f16_f32 v5, v8, v9
	v_cvt_pk_f16_f32 v4, v6, v7
	ds_read_b128 v[6:9], v0 offset:40960
	v_max_f32_e32 v20, 0, v2
	v_cvt_pk_f16_f32 v3, v11, v12
	v_cvt_pk_f16_f32 v2, v1, v10
	v_accvgpr_read_b32 v1, a64
	s_waitcnt lgkmcnt(0)
	v_mfma_f32_32x32x16_f16 a[80:95], v[6:9], v[2:5], 0
	ds_read_b128 v[6:9], v0 offset:41984
	v_cvt_pk_f16_f32 v5, v19, v20
	v_cvt_pk_f16_f32 v4, v17, v18
	v_cvt_pk_f16_f32 v3, v15, v16
	v_cvt_pk_f16_f32 v2, v13, v14
	v_accvgpr_read_b32 v13, a72
	v_accvgpr_read_b32 v17, a76
	s_waitcnt lgkmcnt(0)
	v_mfma_f32_32x32x16_f16 a[80:95], v[6:9], v[2:5], a[80:95]
	ds_read_b128 v[2:5], v22 offset:53376
	v_accvgpr_read_b32 v9, a68
	s_waitcnt lgkmcnt(0)
	v_add_f32_e32 v1, v1, v2
	v_accvgpr_read_b32 v2, a65
	v_add_f32_e32 v2, v3, v2
	v_max_f32_e32 v6, 0, v2
	v_accvgpr_read_b32 v2, a66
	v_add_f32_e32 v2, v4, v2
	v_max_f32_e32 v7, 0, v2
	v_accvgpr_read_b32 v2, a67
	v_add_f32_e32 v2, v5, v2
	v_max_f32_e32 v8, 0, v2
	ds_read_b128 v[2:5], v22 offset:53408
	v_max_f32_e32 v1, 0, v1
	s_waitcnt lgkmcnt(0)
	v_add_f32_e32 v2, v9, v2
	v_max_f32_e32 v9, 0, v2
	v_accvgpr_read_b32 v2, a69
	v_add_f32_e32 v2, v3, v2
	v_max_f32_e32 v10, 0, v2
	v_accvgpr_read_b32 v2, a70
	v_add_f32_e32 v2, v4, v2
	v_max_f32_e32 v11, 0, v2
	v_accvgpr_read_b32 v2, a71
	v_add_f32_e32 v2, v5, v2
	v_max_f32_e32 v12, 0, v2
	ds_read_b128 v[2:5], v22 offset:53440
	s_waitcnt lgkmcnt(0)
	v_add_f32_e32 v2, v13, v2
	v_max_f32_e32 v13, 0, v2
	v_accvgpr_read_b32 v2, a73
	v_add_f32_e32 v2, v3, v2
	v_max_f32_e32 v14, 0, v2
	v_accvgpr_read_b32 v2, a74
	v_add_f32_e32 v2, v4, v2
	v_max_f32_e32 v15, 0, v2
	v_accvgpr_read_b32 v2, a75
	v_add_f32_e32 v2, v5, v2
	v_max_f32_e32 v16, 0, v2
	ds_read_b128 v[2:5], v22 offset:53472
	s_waitcnt lgkmcnt(0)
	v_add_f32_e32 v2, v17, v2
	v_max_f32_e32 v17, 0, v2
	v_accvgpr_read_b32 v2, a77
	v_add_f32_e32 v2, v3, v2
	v_max_f32_e32 v18, 0, v2
	v_accvgpr_read_b32 v2, a78
	v_add_f32_e32 v2, v4, v2
	v_max_f32_e32 v19, 0, v2
	v_accvgpr_read_b32 v2, a79
	v_add_f32_e32 v2, v5, v2
	v_max_f32_e32 v20, 0, v2
	v_cvt_pk_f16_f32 v4, v9, v10
	v_cvt_pk_f16_f32 v3, v7, v8
	v_cvt_pk_f16_f32 v2, v1, v6
	ds_read_b128 v[6:9], v0 offset:43008
	v_cvt_pk_f16_f32 v5, v11, v12
	v_accvgpr_read_b32 v1, a48
	s_waitcnt lgkmcnt(0)
	v_mfma_f32_32x32x16_f16 a[80:95], v[6:9], v[2:5], a[80:95]
	ds_read_b128 v[6:9], v0 offset:44032
	v_cvt_pk_f16_f32 v5, v19, v20
	v_cvt_pk_f16_f32 v4, v17, v18
	v_cvt_pk_f16_f32 v3, v15, v16
	v_cvt_pk_f16_f32 v2, v13, v14
	v_accvgpr_read_b32 v13, a56
	v_accvgpr_read_b32 v17, a60
	s_waitcnt lgkmcnt(0)
	v_mfma_f32_32x32x16_f16 a[80:95], v[6:9], v[2:5], a[80:95]
	ds_read_b128 v[2:5], v22 offset:53504
	v_accvgpr_read_b32 v9, a52
	s_waitcnt lgkmcnt(0)
	v_add_f32_e32 v1, v1, v2
	v_accvgpr_read_b32 v2, a49
	v_add_f32_e32 v2, v3, v2
	v_max_f32_e32 v6, 0, v2
	v_accvgpr_read_b32 v2, a50
	v_add_f32_e32 v2, v4, v2
	v_max_f32_e32 v7, 0, v2
	v_accvgpr_read_b32 v2, a51
	v_add_f32_e32 v2, v5, v2
	v_max_f32_e32 v8, 0, v2
	ds_read_b128 v[2:5], v22 offset:53536
	v_max_f32_e32 v1, 0, v1
	s_waitcnt lgkmcnt(0)
	v_add_f32_e32 v2, v9, v2
	v_max_f32_e32 v9, 0, v2
	v_accvgpr_read_b32 v2, a53
	v_add_f32_e32 v2, v3, v2
	v_max_f32_e32 v10, 0, v2
	v_accvgpr_read_b32 v2, a54
	v_add_f32_e32 v2, v4, v2
	v_max_f32_e32 v11, 0, v2
	v_accvgpr_read_b32 v2, a55
	v_add_f32_e32 v2, v5, v2
	v_max_f32_e32 v12, 0, v2
	ds_read_b128 v[2:5], v22 offset:53568
	s_waitcnt lgkmcnt(0)
	v_add_f32_e32 v2, v13, v2
	v_max_f32_e32 v13, 0, v2
	v_accvgpr_read_b32 v2, a57
	v_add_f32_e32 v2, v3, v2
	v_max_f32_e32 v14, 0, v2
	v_accvgpr_read_b32 v2, a58
	v_add_f32_e32 v2, v4, v2
	v_max_f32_e32 v15, 0, v2
	v_accvgpr_read_b32 v2, a59
	v_add_f32_e32 v2, v5, v2
	v_max_f32_e32 v16, 0, v2
	ds_read_b128 v[2:5], v22 offset:53600
	s_waitcnt lgkmcnt(0)
	v_add_f32_e32 v2, v17, v2
	v_max_f32_e32 v17, 0, v2
	v_accvgpr_read_b32 v2, a61
	v_add_f32_e32 v2, v3, v2
	v_max_f32_e32 v18, 0, v2
	v_accvgpr_read_b32 v2, a62
	v_add_f32_e32 v2, v4, v2
	v_max_f32_e32 v19, 0, v2
	v_accvgpr_read_b32 v2, a63
	v_add_f32_e32 v2, v5, v2
	v_max_f32_e32 v20, 0, v2
	v_cvt_pk_f16_f32 v4, v9, v10
	v_cvt_pk_f16_f32 v3, v7, v8
	v_cvt_pk_f16_f32 v2, v1, v6
	ds_read_b128 v[6:9], v0 offset:45056
	v_cvt_pk_f16_f32 v5, v11, v12
	v_accvgpr_read_b32 v1, a32
	s_waitcnt lgkmcnt(0)
	v_mfma_f32_32x32x16_f16 a[80:95], v[6:9], v[2:5], a[80:95]
	ds_read_b128 v[6:9], v0 offset:46080
	v_cvt_pk_f16_f32 v5, v19, v20
	v_cvt_pk_f16_f32 v4, v17, v18
	v_cvt_pk_f16_f32 v3, v15, v16
	v_cvt_pk_f16_f32 v2, v13, v14
	v_accvgpr_read_b32 v13, a40
	v_accvgpr_read_b32 v17, a44
	s_waitcnt lgkmcnt(0)
	v_mfma_f32_32x32x16_f16 a[80:95], v[6:9], v[2:5], a[80:95]
	ds_read_b128 v[2:5], v22 offset:53632
	v_accvgpr_read_b32 v9, a36
	s_waitcnt lgkmcnt(0)
	v_add_f32_e32 v1, v1, v2
	v_accvgpr_read_b32 v2, a33
	v_add_f32_e32 v2, v3, v2
	v_max_f32_e32 v6, 0, v2
	v_accvgpr_read_b32 v2, a34
	v_add_f32_e32 v2, v4, v2
	v_max_f32_e32 v7, 0, v2
	v_accvgpr_read_b32 v2, a35
	v_add_f32_e32 v2, v5, v2
	v_max_f32_e32 v8, 0, v2
	ds_read_b128 v[2:5], v22 offset:53664
	v_max_f32_e32 v1, 0, v1
	s_waitcnt lgkmcnt(0)
	v_add_f32_e32 v2, v9, v2
	v_max_f32_e32 v9, 0, v2
	v_accvgpr_read_b32 v2, a37
	v_add_f32_e32 v2, v3, v2
	v_max_f32_e32 v10, 0, v2
	v_accvgpr_read_b32 v2, a38
	v_add_f32_e32 v2, v4, v2
	v_max_f32_e32 v11, 0, v2
	v_accvgpr_read_b32 v2, a39
	v_add_f32_e32 v2, v5, v2
	v_max_f32_e32 v12, 0, v2
	ds_read_b128 v[2:5], v22 offset:53696
	s_waitcnt lgkmcnt(0)
	v_add_f32_e32 v2, v13, v2
	v_max_f32_e32 v13, 0, v2
	v_accvgpr_read_b32 v2, a41
	v_add_f32_e32 v2, v3, v2
	v_max_f32_e32 v14, 0, v2
	v_accvgpr_read_b32 v2, a42
	v_add_f32_e32 v2, v4, v2
	v_max_f32_e32 v15, 0, v2
	v_accvgpr_read_b32 v2, a43
	v_add_f32_e32 v2, v5, v2
	v_max_f32_e32 v16, 0, v2
	ds_read_b128 v[2:5], v22 offset:53728
	s_waitcnt lgkmcnt(0)
	v_add_f32_e32 v2, v17, v2
	v_max_f32_e32 v17, 0, v2
	v_accvgpr_read_b32 v2, a45
	v_add_f32_e32 v2, v3, v2
	v_max_f32_e32 v18, 0, v2
	v_accvgpr_read_b32 v2, a46
	v_add_f32_e32 v2, v4, v2
	v_max_f32_e32 v19, 0, v2
	v_accvgpr_read_b32 v2, a47
	v_add_f32_e32 v2, v5, v2
	v_max_f32_e32 v20, 0, v2
	v_cvt_pk_f16_f32 v4, v9, v10
	v_cvt_pk_f16_f32 v3, v7, v8
	v_cvt_pk_f16_f32 v2, v1, v6
	ds_read_b128 v[6:9], v0 offset:47104
	v_cvt_pk_f16_f32 v5, v11, v12
	v_accvgpr_read_b32 v1, a16
	s_waitcnt lgkmcnt(0)
	v_mfma_f32_32x32x16_f16 a[32:47], v[6:9], v[2:5], 0
	ds_read_b128 v[6:9], v0 offset:48128
	v_cvt_pk_f16_f32 v5, v19, v20
	v_cvt_pk_f16_f32 v4, v17, v18
	v_cvt_pk_f16_f32 v3, v15, v16
	v_cvt_pk_f16_f32 v2, v13, v14
	v_accvgpr_read_b32 v13, a24
	v_accvgpr_read_b32 v17, a28
	s_waitcnt lgkmcnt(0)
	v_mfma_f32_32x32x16_f16 a[32:47], v[6:9], v[2:5], a[32:47]
	ds_read_b128 v[2:5], v22 offset:53760
	v_accvgpr_read_b32 v9, a20
	s_waitcnt lgkmcnt(0)
	v_add_f32_e32 v1, v1, v2
	v_accvgpr_read_b32 v2, a17
	v_add_f32_e32 v2, v3, v2
	v_max_f32_e32 v6, 0, v2
	v_accvgpr_read_b32 v2, a18
	v_add_f32_e32 v2, v4, v2
	v_max_f32_e32 v7, 0, v2
	v_accvgpr_read_b32 v2, a19
	v_add_f32_e32 v2, v5, v2
	v_max_f32_e32 v8, 0, v2
	ds_read_b128 v[2:5], v22 offset:53792
	v_max_f32_e32 v1, 0, v1
	s_waitcnt lgkmcnt(0)
	v_add_f32_e32 v2, v9, v2
	v_max_f32_e32 v9, 0, v2
	v_accvgpr_read_b32 v2, a21
	v_add_f32_e32 v2, v3, v2
	v_max_f32_e32 v10, 0, v2
	v_accvgpr_read_b32 v2, a22
	v_add_f32_e32 v2, v4, v2
	v_max_f32_e32 v11, 0, v2
	v_accvgpr_read_b32 v2, a23
	v_add_f32_e32 v2, v5, v2
	v_max_f32_e32 v12, 0, v2
	ds_read_b128 v[2:5], v22 offset:53824
	s_waitcnt lgkmcnt(0)
	v_add_f32_e32 v2, v13, v2
	v_max_f32_e32 v13, 0, v2
	v_accvgpr_read_b32 v2, a25
	v_add_f32_e32 v2, v3, v2
	v_max_f32_e32 v14, 0, v2
	v_accvgpr_read_b32 v2, a26
	v_add_f32_e32 v2, v4, v2
	v_max_f32_e32 v15, 0, v2
	v_accvgpr_read_b32 v2, a27
	v_add_f32_e32 v2, v5, v2
	v_max_f32_e32 v16, 0, v2
	ds_read_b128 v[2:5], v22 offset:53856
	s_waitcnt lgkmcnt(0)
	v_add_f32_e32 v2, v17, v2
	v_max_f32_e32 v17, 0, v2
	v_accvgpr_read_b32 v2, a29
	v_add_f32_e32 v2, v3, v2
	v_max_f32_e32 v18, 0, v2
	v_accvgpr_read_b32 v2, a30
	v_add_f32_e32 v2, v4, v2
	v_max_f32_e32 v19, 0, v2
	v_accvgpr_read_b32 v2, a31
	v_add_f32_e32 v2, v5, v2
	v_max_f32_e32 v20, 0, v2
	v_cvt_pk_f16_f32 v4, v9, v10
	v_cvt_pk_f16_f32 v3, v7, v8
	v_cvt_pk_f16_f32 v2, v1, v6
	ds_read_b128 v[6:9], v0 offset:49152
	v_cvt_pk_f16_f32 v5, v11, v12
	v_accvgpr_read_b32 v1, a0
	s_waitcnt lgkmcnt(0)
	v_mfma_f32_32x32x16_f16 a[32:47], v[6:9], v[2:5], a[32:47]
	ds_read_b128 v[6:9], v0 offset:50176
	v_cvt_pk_f16_f32 v5, v19, v20
	v_cvt_pk_f16_f32 v4, v17, v18
	v_cvt_pk_f16_f32 v3, v15, v16
	v_cvt_pk_f16_f32 v2, v13, v14
	v_accvgpr_read_b32 v13, a8
	v_accvgpr_read_b32 v17, a12
	s_waitcnt lgkmcnt(0)
	v_mfma_f32_32x32x16_f16 a[32:47], v[6:9], v[2:5], a[32:47]
	ds_read_b128 v[2:5], v22 offset:53888
	v_accvgpr_read_b32 v9, a4
	s_waitcnt lgkmcnt(0)
	v_add_f32_e32 v1, v1, v2
	v_accvgpr_read_b32 v2, a1
	v_add_f32_e32 v2, v3, v2
	v_max_f32_e32 v6, 0, v2
	v_accvgpr_read_b32 v2, a2
	v_add_f32_e32 v2, v4, v2
	v_max_f32_e32 v7, 0, v2
	v_accvgpr_read_b32 v2, a3
	v_add_f32_e32 v2, v5, v2
	v_max_f32_e32 v8, 0, v2
	ds_read_b128 v[2:5], v22 offset:53920
	v_max_f32_e32 v1, 0, v1
	s_waitcnt lgkmcnt(0)
	v_add_f32_e32 v2, v9, v2
	v_max_f32_e32 v9, 0, v2
	v_accvgpr_read_b32 v2, a5
	v_add_f32_e32 v2, v3, v2
	v_max_f32_e32 v10, 0, v2
	v_accvgpr_read_b32 v2, a6
	v_add_f32_e32 v2, v4, v2
	v_max_f32_e32 v11, 0, v2
	v_accvgpr_read_b32 v2, a7
	v_add_f32_e32 v2, v5, v2
	v_max_f32_e32 v12, 0, v2
	ds_read_b128 v[2:5], v22 offset:53952
	s_waitcnt lgkmcnt(0)
	v_add_f32_e32 v2, v13, v2
	v_max_f32_e32 v13, 0, v2
	v_accvgpr_read_b32 v2, a9
	v_add_f32_e32 v2, v3, v2
	v_max_f32_e32 v14, 0, v2
	v_accvgpr_read_b32 v2, a10
	v_add_f32_e32 v2, v4, v2
	v_max_f32_e32 v15, 0, v2
	v_accvgpr_read_b32 v2, a11
	v_add_f32_e32 v2, v5, v2
	v_max_f32_e32 v16, 0, v2
	ds_read_b128 v[2:5], v22 offset:53984
	s_waitcnt lgkmcnt(0)
	v_add_f32_e32 v2, v17, v2
	v_max_f32_e32 v17, 0, v2
	v_accvgpr_read_b32 v2, a13
	v_add_f32_e32 v2, v3, v2
	v_max_f32_e32 v18, 0, v2
	v_accvgpr_read_b32 v2, a14
	v_add_f32_e32 v2, v4, v2
	v_max_f32_e32 v19, 0, v2
	v_accvgpr_read_b32 v2, a15
	v_add_f32_e32 v2, v5, v2
	v_max_f32_e32 v20, 0, v2
	v_cvt_pk_f16_f32 v4, v9, v10
	v_cvt_pk_f16_f32 v3, v7, v8
	v_cvt_pk_f16_f32 v2, v1, v6
	ds_read_b128 v[6:9], v0 offset:51200
	v_cvt_pk_f16_f32 v5, v11, v12
	s_waitcnt lgkmcnt(0)
	s_nop 0
	v_mfma_f32_32x32x16_f16 a[32:47], v[6:9], v[2:5], a[32:47]
	ds_read_b128 v[6:9], v0 offset:52224
	v_cvt_pk_f16_f32 v5, v19, v20
	v_cvt_pk_f16_f32 v4, v17, v18
	v_cvt_pk_f16_f32 v3, v15, v16
	v_cvt_pk_f16_f32 v2, v13, v14
	s_waitcnt lgkmcnt(0)
	s_nop 0
	v_mfma_f32_32x32x16_f16 a[32:47], v[6:9], v[2:5], a[32:47]
	s_and_saveexec_b64 s[2:3], s[0:1]
	s_cbranch_execz .LBB3_39
	v_accvgpr_read_b32 v0, a80
	v_accvgpr_read_b32 v6, a86
	v_accvgpr_read_b32 v7, a87
	v_accvgpr_read_b32 v8, a88
	v_accvgpr_read_b32 v9, a89
	v_accvgpr_read_b32 v10, a90
	v_accvgpr_read_b32 v11, a91
	v_accvgpr_read_b32 v12, a92
	v_accvgpr_read_b32 v13, a93
	v_accvgpr_read_b32 v14, a94
	v_accvgpr_read_b32 v15, a95
	v_accvgpr_read_b32 v6, a32
	v_accvgpr_read_b32 v14, a40
	v_accvgpr_read_b32 v15, a41
	v_accvgpr_read_b32 v16, a42
	v_accvgpr_read_b32 v17, a43
	v_accvgpr_read_b32 v18, a44
	v_accvgpr_read_b32 v19, a45
	v_accvgpr_read_b32 v20, a46
	v_accvgpr_read_b32 v21, a47
	ds_read_b128 v[14:17], v22 offset:54016
	ds_read_b128 v[18:21], v22 offset:54080
	v_accvgpr_read_b32 v12, a38
	v_accvgpr_read_b32 v13, a39
	v_lshlrev_b32_e32 v24, 2, v85
	v_accvgpr_read_b32 v1, a81
	v_accvgpr_read_b32 v7, a33
	v_mad_i64_i32 v[12:13], s[0:1], v80, 40, s[18:19]
	v_ashrrev_i32_e32 v25, 31, v24
	v_accvgpr_read_b32 v3, a83
	v_accvgpr_read_b32 v9, a35
	v_lshl_add_u64 v[22:23], v[24:25], 2, v[12:13]
	v_mov_b32_e32 v25, v1
	s_waitcnt lgkmcnt(1)
	v_mov_b32_e32 v27, v15
	v_mov_b32_e32 v1, v7
	s_waitcnt lgkmcnt(0)
	v_mov_b32_e32 v15, v19
	v_accvgpr_read_b32 v2, a82
	v_accvgpr_read_b32 v8, a34
	v_pk_add_f32 v[0:1], v[0:1], v[14:15]
	v_mov_b32_e32 v7, v3
	v_mov_b32_e32 v15, v17
	v_mov_b32_e32 v3, v9
	v_mov_b32_e32 v17, v21
	v_mov_b32_e32 v24, v6
	v_mov_b32_e32 v26, v18
	v_mov_b32_e32 v6, v8
	v_mov_b32_e32 v14, v20
	v_pk_add_f32 v[2:3], v[2:3], v[16:17]
	v_pk_add_f32 v[24:25], v[24:25], v[26:27]
	s_waitcnt vmcnt(0)
	v_pk_mul_f32 v[0:1], v[82:83], v[0:1]
	v_pk_add_f32 v[6:7], v[6:7], v[14:15]
	v_pk_mul_f32 v[2:3], v[82:83], v[2:3]
	v_accvgpr_read_b32 v4, a84
	v_accvgpr_read_b32 v5, a85
	v_accvgpr_read_b32 v10, a36
	v_accvgpr_read_b32 v11, a37
	v_pk_fma_f32 v[0:1], v[82:83], v[24:25], v[0:1] op_sel:[1,0,0] op_sel_hi:[0,1,1]
	v_pk_fma_f32 v[2:3], v[82:83], v[6:7], v[2:3] op_sel:[1,0,0] op_sel_hi:[0,1,1]
	v_cmp_eq_u32_e32 vcc, 0, v85
	global_store_dwordx4 v[22:23], v[0:3], off
	s_and_b64 exec, exec, vcc
	s_cbranch_execz .LBB3_39
	s_mov_b32 s0, 0xd000
	v_add_u32_e64 v0, s0, 0
	ds_read2_b64 v[0:3], v0 offset0:100 offset1:108
	v_mov_b32_e32 v9, v5
	v_mov_b32_e32 v5, v11
	v_mov_b32_e32 v8, v10
	v_pk_mov_b32 v[6:7], v[82:83], v[82:83] op_sel:[1,0]
	s_waitcnt lgkmcnt(0)
	v_mov_b32_e32 v15, v1
	v_mov_b32_e32 v1, v3
	v_mov_b32_e32 v14, v2
	v_pk_add_f32 v[0:1], v[4:5], v[0:1]
	v_pk_add_f32 v[8:9], v[8:9], v[14:15]
	v_pk_mul_f32 v[0:1], v[82:83], v[0:1]
	s_nop 0
	v_pk_fma_f32 v[0:1], v[6:7], v[8:9], v[0:1]
	global_store_dwordx2 v[12:13], v[0:1], off offset:32
